# attn loop1 drops per-tile max (block-wide end check + exact redo path); loop2 second copy without S2 max-subtract when all |m2|<=100 (nl2 scaled by 2^-m2), aligned
# speedup vs baseline: 1.0317x; 1.0317x over previous
.LBB4_2:
	s_mov_b32 s32, s0
	s_mov_b32 s33, s1
	s_mov_b32 s34, s3
	s_mov_b32 s35, s4
	s_mov_b32 s36, s5
	s_mov_b32 s37, 0
	s_mov_b32 s26, 0x71800000
	s_mov_b32 s27, 0x0d800000
	v_mov_b32_e32 v85, 0x12000
	v_mov_b32_e32 v86, 0
	ds_write_b32 v85, v86
.Lp_top:
	s_lshl_b32 s6, s21, 20
	s_add_u32 s4, s4, s6
	s_addc_u32 s5, s5, 0
	v_lshlrev_b32_e32 v54, 4, v0
	v_mov_b32_e32 v55, v63
	s_lshl_b32 s3, s3, 1
	s_mul_i32 s20, s21, 5
	v_lshl_add_u64 v[4:5], s[4:5], 0, v[54:55]
	s_mov_b64 s[4:5], 0x1000000
	s_add_i32 s20, s20, s3
	v_lshl_add_u64 v[170:171], v[4:5], 0, s[4:5]
	s_and_b32 s22, s20, 31
	s_lshl_b32 s4, s20, 12
	s_lshl_b32 s12, s22, 13
	s_add_i32 s5, s4, 0x1000
	v_lshl_add_u64 v[58:59], v[170:171], 0, s[12:13]
	s_mov_b32 s3, 0x80000
	s_and_b32 s5, s5, 0x1f000
	v_add_co_u32_e32 v16, vcc, s3, v58
	s_lshl_b32 s12, s5, 1
	s_nop 0
	v_addc_co_u32_e32 v17, vcc, 0, v59, vcc
	v_lshl_add_u64 v[56:57], v[170:171], 0, s[12:13]
	global_load_dwordx4 v[4:7], v[58:59], off
	global_load_dwordx4 v[8:11], v[56:57], off
	global_load_dwordx4 v[12:15], v[16:17], off
	v_add_co_u32_e32 v16, vcc, s3, v56
	v_lshrrev_b32_e32 v184, 8, v0
	s_nop 0
	v_addc_co_u32_e32 v17, vcc, 0, v57, vcc
	global_load_dwordx4 v[16:19], v[16:17], off
	v_and_b32_e32 v20, 19, v0
	v_lshlrev_b32_e32 v21, 1, v0
	v_and_b32_e32 v2, 4, v2
	v_and_or_b32 v20, v21, 8, v20
	v_lshlrev_b32_e32 v101, 5, v184
	s_addk_i32 s4, 0x2000
	v_or3_b32 v2, v20, v2, v101
	s_and_b32 s4, s4, 0x1f000
	v_mul_u32_u24_e32 v2, 0x48, v2
	s_lshl_b32 s12, s4, 1
	v_lshlrev_b32_e32 v3, 3, v0
	v_lshlrev_b32_e32 v100, 1, v99
	v_lshlrev_b32_e32 v2, 1, v2
	v_lshl_add_u64 v[60:61], v[170:171], 0, s[12:13]
	v_and_b32_e32 v3, 56, v3
	v_add3_u32 v186, 0, v2, v100
	v_add_co_u32_e32 v2, vcc, s3, v60
	v_lshlrev_b32_e32 v68, 1, v3
	s_nop 0
	v_addc_co_u32_e32 v3, vcc, 0, v61, vcc
	global_load_dwordx4 v[162:165], v[60:61], off
	global_load_dwordx4 v[166:169], v[2:3], off
	v_lshrrev_b32_e32 v82, 3, v0
	v_mul_u32_u24_e32 v22, 0x48, v82
	v_lshlrev_b32_e32 v21, 1, v22
	v_add3_u32 v185, 0, v21, v68
	s_mov_b64 s[24:25], 0x80000
	s_add_i32 s17, s20, 3
	s_add_i32 s18, s20, 4
	v_mov_b32_e32 v62, v63
	v_lshrrev_b32_e32 v55, 6, v0
	v_mov_b32_e32 v83, 0
	v_mov_b32_e32 v84, 0
	v_lshl_add_u64 v[70:71], v[58:59], 0, s[24:25]
	v_lshl_add_u64 v[66:67], v[56:57], 0, s[24:25]
	v_lshl_add_u64 v[64:65], v[60:61], 0, s[24:25]
	s_waitcnt vmcnt(5)
	ds_write_b128 v185, v[4:7]
	s_waitcnt vmcnt(3)
	ds_write_b128 v185, v[12:15] offset:9216
	ds_write_b128 v185, v[8:11] offset:18432
	s_waitcnt vmcnt(2)
	ds_write_b128 v185, v[16:19] offset:27648
	s_waitcnt lgkmcnt(0)
	s_barrier
	ds_read_b128 v[2:5], v186
	ds_read_b128 v[38:41], v186 offset:32
	s_waitcnt lgkmcnt(1)
	v_mfma_f32_32x32x16_f16 v[2:17], v[2:5], v[114:117], 0
	ds_read_b128 v[18:21], v186 offset:9216
	ds_read_b128 v[46:49], v186 offset:9248
	s_waitcnt lgkmcnt(1)
	v_mfma_f32_32x32x16_f16 v[18:33], v[18:21], v[130:133], 0
	v_mfma_f32_32x32x16_f16 v[2:17], v[38:41], v[118:121], v[2:17]
	s_waitcnt lgkmcnt(0)
	v_mfma_f32_32x32x16_f16 v[18:33], v[46:49], v[134:137], v[18:33]
	ds_read_b128 v[38:41], v186 offset:64
	ds_read_b128 v[46:49], v186 offset:96
	s_waitcnt lgkmcnt(1)
	v_mfma_f32_32x32x16_f16 v[2:17], v[38:41], v[122:125], v[2:17]
	ds_read_b128 v[38:41], v186 offset:9280
	ds_read_b128 v[50:53], v186 offset:9312
	s_load_dwordx4 s[4:7], s[0:1], 0x38
	s_load_dwordx2 s[14:15], s[0:1], 0x8
	s_mov_b32 s0, -2
	s_mov_b32 s1, 0x3f800000
	s_waitcnt lgkmcnt(0)
	s_barrier
	v_mfma_f32_32x32x16_f16 v[18:33], v[38:41], v[138:141], v[18:33]
	v_mfma_f32_32x32x16_f16 v[2:17], v[46:49], v[126:129], v[2:17]
	v_mfma_f32_32x32x16_f16 v[18:33], v[50:53], v[142:145], v[18:33]
	s_nop 7
	s_cmp_eq_u32 s37, 1
	s_cbranch_scc0 .Lf_A
	v_mov_b32_e32 v83, 0xf149f2ca
	v_mov_b32_e32 v84, 0xf149f2ca
	s_branch .Ls_A
.Lf_A:
	s_add_i32 s0, s0, 2
	ds_read_b128 v[102:105], v186 offset:18432
	ds_read_b128 v[106:109], v186 offset:27648
	ds_read_b128 v[110:113], v186 offset:18464
	ds_read_b128 v[86:89], v186 offset:27680
	ds_read_b128 v[90:93], v186 offset:18496
	ds_read_b128 v[172:175], v186 offset:27712
	ds_read_b128 v[72:75], v186 offset:18528
	v_exp_f32_e32 v2, v2
	v_exp_f32_e32 v18, v18
	s_waitcnt lgkmcnt(6)
	v_mfma_f32_32x32x16_f16 v[146:161], v[102:105], v[114:117], 0
	v_exp_f32_e32 v3, v3
	v_exp_f32_e32 v19, v19
	v_exp_f32_e32 v4, v4
	v_exp_f32_e32 v20, v20
	s_waitcnt lgkmcnt(5)
	v_mfma_f32_32x32x16_f16 v[34:49], v[106:109], v[130:133], 0
	v_exp_f32_e32 v5, v5
	v_exp_f32_e32 v21, v21
	v_exp_f32_e32 v6, v6
	v_exp_f32_e32 v22, v22
	s_waitcnt lgkmcnt(4)
	v_mfma_f32_32x32x16_f16 v[146:161], v[110:113], v[118:121], v[146:161]
	v_exp_f32_e32 v7, v7
	v_exp_f32_e32 v23, v23
	v_exp_f32_e32 v8, v8
	v_exp_f32_e32 v24, v24
	s_waitcnt lgkmcnt(3)
	v_mfma_f32_32x32x16_f16 v[34:49], v[86:89], v[134:137], v[34:49]
	v_exp_f32_e32 v9, v9
	v_exp_f32_e32 v25, v25
	s_waitcnt vmcnt(0)
	ds_write_b128 v185, v[162:165]
	ds_write_b128 v185, v[166:169] offset:9216
	ds_read_b128 v[162:165], v186 offset:27744
	s_min_u32 s12, s0, 28
	s_add_i32 s12, s17, s12
	s_lshl_b32 s12, s12, 13
	s_and_b32 s12, s12, 0x3e000
	s_add_u32 s28, s12, s3
	s_mov_b32 s29, 0
	v_lshl_add_u64 v[176:177], v[170:171], 0, s[12:13]
	global_load_dwordx4 v[50:53], v[176:177], off
	v_lshl_add_u64 v[176:177], v[170:171], 0, s[28:29]
	global_load_dwordx4 v[94:97], v[176:177], off
	v_exp_f32_e32 v10, v10
	v_exp_f32_e32 v26, v26
	v_exp_f32_e32 v11, v11
	v_exp_f32_e32 v27, v27
	s_waitcnt lgkmcnt(5)
	v_mfma_f32_32x32x16_f16 v[146:161], v[90:93], v[122:125], v[146:161]
	v_exp_f32_e32 v12, v12
	v_exp_f32_e32 v28, v28
	v_exp_f32_e32 v13, v13
	v_exp_f32_e32 v29, v29
	s_waitcnt lgkmcnt(4)
	v_mfma_f32_32x32x16_f16 v[34:49], v[172:175], v[138:141], v[34:49]
	v_exp_f32_e32 v14, v14
	v_exp_f32_e32 v30, v30
	v_exp_f32_e32 v15, v15
	v_exp_f32_e32 v31, v31
	s_waitcnt lgkmcnt(3)
	v_mfma_f32_32x32x16_f16 v[146:161], v[72:75], v[126:129], v[146:161]
	v_exp_f32_e32 v16, v16
	v_exp_f32_e32 v32, v32
	v_exp_f32_e32 v17, v17
	v_exp_f32_e32 v33, v33
	v_add_f32_e32 v2, v2, v3
	v_add_f32_e32 v4, v4, v5
	v_add_f32_e32 v6, v6, v7
	v_add_f32_e32 v8, v8, v9
	v_add_f32_e32 v10, v10, v11
	v_add_f32_e32 v12, v12, v13
	v_add_f32_e32 v14, v14, v15
	v_add_f32_e32 v16, v16, v17
	v_add_f32_e32 v18, v18, v19
	v_add_f32_e32 v20, v20, v21
	s_waitcnt lgkmcnt(0)
	v_mfma_f32_32x32x16_f16 v[34:49], v[162:165], v[142:145], v[34:49]
	v_add_f32_e32 v22, v22, v23
	v_add_f32_e32 v24, v24, v25
	v_add_f32_e32 v26, v26, v27
	v_add_f32_e32 v28, v28, v29
	v_add_f32_e32 v30, v30, v31
	v_add_f32_e32 v32, v32, v33
	v_add_f32_e32 v2, v2, v4
	v_add_f32_e32 v6, v6, v8
	v_add_f32_e32 v10, v10, v12
	v_add_f32_e32 v14, v14, v16
	v_add_f32_e32 v18, v18, v20
	v_add_f32_e32 v22, v22, v24
	v_add_f32_e32 v26, v26, v28
	v_add_f32_e32 v30, v30, v32
	v_add_f32_e32 v2, v2, v6
	v_add_f32_e32 v10, v10, v14
	v_add_f32_e32 v18, v18, v22
	v_add_f32_e32 v26, v26, v30
	v_add_f32_e32 v2, v2, v10
	v_add_f32_e32 v18, v18, v26
	v_add_f32_e32 v63, v63, v2
	v_add_f32_e32 v62, v62, v18
	s_waitcnt lgkmcnt(0)
	s_barrier
.Lf_B:
	ds_read_b128 v[102:105], v186
	ds_read_b128 v[106:109], v186 offset:9216
	ds_read_b128 v[110:113], v186 offset:32
	ds_read_b128 v[86:89], v186 offset:9248
	ds_read_b128 v[90:93], v186 offset:64
	ds_read_b128 v[172:175], v186 offset:9280
	ds_read_b128 v[72:75], v186 offset:96
	v_exp_f32_e32 v146, v146
	v_exp_f32_e32 v34, v34
	s_waitcnt lgkmcnt(6)
	v_mfma_f32_32x32x16_f16 v[2:17], v[102:105], v[114:117], 0
	v_exp_f32_e32 v147, v147
	v_exp_f32_e32 v35, v35
	v_exp_f32_e32 v148, v148
	v_exp_f32_e32 v36, v36
	s_waitcnt lgkmcnt(5)
	v_mfma_f32_32x32x16_f16 v[18:33], v[106:109], v[130:133], 0
	v_exp_f32_e32 v149, v149
	v_exp_f32_e32 v37, v37
	v_exp_f32_e32 v150, v150
	v_exp_f32_e32 v38, v38
	s_waitcnt lgkmcnt(4)
	v_mfma_f32_32x32x16_f16 v[2:17], v[110:113], v[118:121], v[2:17]
	v_exp_f32_e32 v151, v151
	v_exp_f32_e32 v39, v39
	v_exp_f32_e32 v152, v152
	v_exp_f32_e32 v40, v40
	s_waitcnt lgkmcnt(3)
	v_mfma_f32_32x32x16_f16 v[18:33], v[86:89], v[134:137], v[18:33]
	v_exp_f32_e32 v153, v153
	v_exp_f32_e32 v41, v41
	s_waitcnt vmcnt(0)
	ds_write_b128 v185, v[50:53] offset:18432
	ds_write_b128 v185, v[94:97] offset:27648
	ds_read_b128 v[50:53], v186 offset:9312
	s_min_u32 s12, s0, 27
	s_add_i32 s12, s18, s12
	s_lshl_b32 s12, s12, 13
	s_and_b32 s12, s12, 0x3e000
	s_add_u32 s28, s12, s3
	s_mov_b32 s29, 0
	v_lshl_add_u64 v[176:177], v[170:171], 0, s[12:13]
	global_load_dwordx4 v[162:165], v[176:177], off
	v_lshl_add_u64 v[176:177], v[170:171], 0, s[28:29]
	global_load_dwordx4 v[166:169], v[176:177], off
	v_exp_f32_e32 v154, v154
	v_exp_f32_e32 v42, v42
	v_exp_f32_e32 v155, v155
	v_exp_f32_e32 v43, v43
	s_waitcnt lgkmcnt(5)
	v_mfma_f32_32x32x16_f16 v[2:17], v[90:93], v[122:125], v[2:17]
	v_exp_f32_e32 v156, v156
	v_exp_f32_e32 v44, v44
	v_exp_f32_e32 v157, v157
	v_exp_f32_e32 v45, v45
	s_waitcnt lgkmcnt(4)
	v_mfma_f32_32x32x16_f16 v[18:33], v[172:175], v[138:141], v[18:33]
	v_exp_f32_e32 v158, v158
	v_exp_f32_e32 v46, v46
	v_exp_f32_e32 v159, v159
	v_exp_f32_e32 v47, v47
	s_waitcnt lgkmcnt(3)
	v_mfma_f32_32x32x16_f16 v[2:17], v[72:75], v[126:129], v[2:17]
	v_exp_f32_e32 v160, v160
	v_exp_f32_e32 v48, v48
	v_exp_f32_e32 v161, v161
	v_exp_f32_e32 v49, v49
	v_add_f32_e32 v146, v146, v147
	v_add_f32_e32 v148, v148, v149
	v_add_f32_e32 v150, v150, v151
	v_add_f32_e32 v152, v152, v153
	v_add_f32_e32 v154, v154, v155
	v_add_f32_e32 v156, v156, v157
	v_add_f32_e32 v158, v158, v159
	v_add_f32_e32 v160, v160, v161
	v_add_f32_e32 v34, v34, v35
	v_add_f32_e32 v36, v36, v37
	s_waitcnt lgkmcnt(0)
	v_mfma_f32_32x32x16_f16 v[18:33], v[50:53], v[142:145], v[18:33]
	v_add_f32_e32 v38, v38, v39
	v_add_f32_e32 v40, v40, v41
	v_add_f32_e32 v42, v42, v43
	v_add_f32_e32 v44, v44, v45
	v_add_f32_e32 v46, v46, v47
	v_add_f32_e32 v48, v48, v49
	v_add_f32_e32 v146, v146, v148
	v_add_f32_e32 v150, v150, v152
	v_add_f32_e32 v154, v154, v156
	v_add_f32_e32 v158, v158, v160
	v_add_f32_e32 v34, v34, v36
	v_add_f32_e32 v38, v38, v40
	v_add_f32_e32 v42, v42, v44
	v_add_f32_e32 v46, v46, v48
	v_add_f32_e32 v146, v146, v150
	v_add_f32_e32 v154, v154, v158
	v_add_f32_e32 v34, v34, v38
	v_add_f32_e32 v42, v42, v46
	v_add_f32_e32 v146, v146, v154
	v_add_f32_e32 v34, v34, v42
	v_add_f32_e32 v63, v63, v146
	v_add_f32_e32 v62, v62, v34
	s_waitcnt lgkmcnt(0)
	s_barrier
	s_cmp_lt_u32 s0, 30
	s_cbranch_scc1 .Lf_A
	s_branch .Ll1_done
.Ls_A:
	s_add_i32 s0, s0, 2
	ds_read_b128 v[102:105], v186 offset:18432
	ds_read_b128 v[106:109], v186 offset:27648
	ds_read_b128 v[110:113], v186 offset:18464
	ds_read_b128 v[86:89], v186 offset:27680
	ds_read_b128 v[90:93], v186 offset:18496
	ds_read_b128 v[172:175], v186 offset:27712
	ds_read_b128 v[72:75], v186 offset:18528
	v_max3_f32 v76, v2, v3, v4
	v_max3_f32 v77, v18, v19, v20
	v_max3_f32 v76, v76, v5, v6
	v_max3_f32 v77, v77, v21, v22
	v_max3_f32 v76, v76, v7, v8
	v_max3_f32 v77, v77, v23, v24
	v_max3_f32 v76, v76, v9, v10
	v_max3_f32 v77, v77, v25, v26
	v_max3_f32 v76, v76, v11, v12
	v_max3_f32 v77, v77, v27, v28
	v_max3_f32 v76, v76, v13, v14
	v_max3_f32 v77, v77, v29, v30
	v_max3_f32 v76, v76, v15, v16
	v_max3_f32 v77, v77, v31, v32
	v_max_f32_e32 v76, v76, v17
	v_max_f32_e32 v77, v77, v33
	v_max_f32_e32 v85, v84, v76
	v_sub_f32_e32 v76, v84, v85
	v_exp_f32_e32 v76, v76
	v_mov_b32_e32 v84, v85
	v_sub_f32_e32 v2, v2, v85
	v_sub_f32_e32 v3, v3, v85
	v_sub_f32_e32 v4, v4, v85
	v_sub_f32_e32 v5, v5, v85
	v_sub_f32_e32 v6, v6, v85
	v_sub_f32_e32 v7, v7, v85
	v_sub_f32_e32 v8, v8, v85
	v_sub_f32_e32 v9, v9, v85
	v_sub_f32_e32 v10, v10, v85
	v_sub_f32_e32 v11, v11, v85
	v_sub_f32_e32 v12, v12, v85
	v_sub_f32_e32 v13, v13, v85
	v_sub_f32_e32 v14, v14, v85
	v_sub_f32_e32 v15, v15, v85
	v_sub_f32_e32 v16, v16, v85
	v_sub_f32_e32 v17, v17, v85
	v_max_f32_e32 v85, v83, v77
	v_sub_f32_e32 v77, v83, v85
	v_exp_f32_e32 v77, v77
	v_mov_b32_e32 v83, v85
	v_sub_f32_e32 v18, v18, v85
	v_sub_f32_e32 v19, v19, v85
	v_sub_f32_e32 v20, v20, v85
	v_sub_f32_e32 v21, v21, v85
	v_sub_f32_e32 v22, v22, v85
	v_sub_f32_e32 v23, v23, v85
	v_sub_f32_e32 v24, v24, v85
	v_sub_f32_e32 v25, v25, v85
	v_sub_f32_e32 v26, v26, v85
	v_sub_f32_e32 v27, v27, v85
	v_sub_f32_e32 v28, v28, v85
	v_sub_f32_e32 v29, v29, v85
	v_sub_f32_e32 v30, v30, v85
	v_sub_f32_e32 v31, v31, v85
	v_sub_f32_e32 v32, v32, v85
	v_sub_f32_e32 v33, v33, v85
	v_exp_f32_e32 v2, v2
	v_exp_f32_e32 v18, v18
	s_waitcnt lgkmcnt(6)
	v_mfma_f32_32x32x16_f16 v[146:161], v[102:105], v[114:117], 0
	v_exp_f32_e32 v3, v3
	v_exp_f32_e32 v19, v19
	v_exp_f32_e32 v4, v4
	v_exp_f32_e32 v20, v20
	s_waitcnt lgkmcnt(5)
	v_mfma_f32_32x32x16_f16 v[34:49], v[106:109], v[130:133], 0
	v_exp_f32_e32 v5, v5
	v_exp_f32_e32 v21, v21
	v_exp_f32_e32 v6, v6
	v_exp_f32_e32 v22, v22
	s_waitcnt lgkmcnt(4)
	v_mfma_f32_32x32x16_f16 v[146:161], v[110:113], v[118:121], v[146:161]
	v_exp_f32_e32 v7, v7
	v_exp_f32_e32 v23, v23
	v_exp_f32_e32 v8, v8
	v_exp_f32_e32 v24, v24
	s_waitcnt lgkmcnt(3)
	v_mfma_f32_32x32x16_f16 v[34:49], v[86:89], v[134:137], v[34:49]
	v_exp_f32_e32 v9, v9
	v_exp_f32_e32 v25, v25
	s_waitcnt vmcnt(0)
	ds_write_b128 v185, v[162:165]
	ds_write_b128 v185, v[166:169] offset:9216
	ds_read_b128 v[162:165], v186 offset:27744
	s_min_u32 s12, s0, 28
	s_add_i32 s12, s17, s12
	s_lshl_b32 s12, s12, 13
	s_and_b32 s12, s12, 0x3e000
	s_add_u32 s28, s12, s3
	s_mov_b32 s29, 0
	v_lshl_add_u64 v[176:177], v[170:171], 0, s[12:13]
	global_load_dwordx4 v[50:53], v[176:177], off
	v_lshl_add_u64 v[176:177], v[170:171], 0, s[28:29]
	global_load_dwordx4 v[94:97], v[176:177], off
	v_exp_f32_e32 v10, v10
	v_exp_f32_e32 v26, v26
	v_exp_f32_e32 v11, v11
	v_exp_f32_e32 v27, v27
	s_waitcnt lgkmcnt(5)
	v_mfma_f32_32x32x16_f16 v[146:161], v[90:93], v[122:125], v[146:161]
	v_exp_f32_e32 v12, v12
	v_exp_f32_e32 v28, v28
	v_exp_f32_e32 v13, v13
	v_exp_f32_e32 v29, v29
	s_waitcnt lgkmcnt(4)
	v_mfma_f32_32x32x16_f16 v[34:49], v[172:175], v[138:141], v[34:49]
	v_exp_f32_e32 v14, v14
	v_exp_f32_e32 v30, v30
	v_exp_f32_e32 v15, v15
	v_exp_f32_e32 v31, v31
	s_waitcnt lgkmcnt(3)
	v_mfma_f32_32x32x16_f16 v[146:161], v[72:75], v[126:129], v[146:161]
	v_exp_f32_e32 v16, v16
	v_exp_f32_e32 v32, v32
	v_exp_f32_e32 v17, v17
	v_exp_f32_e32 v33, v33
	v_add_f32_e32 v2, v2, v3
	v_add_f32_e32 v4, v4, v5
	v_add_f32_e32 v6, v6, v7
	v_add_f32_e32 v8, v8, v9
	v_add_f32_e32 v10, v10, v11
	v_add_f32_e32 v12, v12, v13
	v_add_f32_e32 v14, v14, v15
	v_add_f32_e32 v16, v16, v17
	v_add_f32_e32 v18, v18, v19
	v_add_f32_e32 v20, v20, v21
	s_waitcnt lgkmcnt(0)
	v_mfma_f32_32x32x16_f16 v[34:49], v[162:165], v[142:145], v[34:49]
	v_add_f32_e32 v22, v22, v23
	v_add_f32_e32 v24, v24, v25
	v_add_f32_e32 v26, v26, v27
	v_add_f32_e32 v28, v28, v29
	v_add_f32_e32 v30, v30, v31
	v_add_f32_e32 v32, v32, v33
	v_add_f32_e32 v2, v2, v4
	v_add_f32_e32 v6, v6, v8
	v_add_f32_e32 v10, v10, v12
	v_add_f32_e32 v14, v14, v16
	v_add_f32_e32 v18, v18, v20
	v_add_f32_e32 v22, v22, v24
	v_add_f32_e32 v26, v26, v28
	v_add_f32_e32 v30, v30, v32
	v_add_f32_e32 v2, v2, v6
	v_add_f32_e32 v10, v10, v14
	v_add_f32_e32 v18, v18, v22
	v_add_f32_e32 v26, v26, v30
	v_add_f32_e32 v2, v2, v10
	v_add_f32_e32 v18, v18, v26
	v_fma_f32 v63, v63, v76, v2
	v_fma_f32 v62, v62, v77, v18
	s_waitcnt lgkmcnt(0)
	s_barrier
.Ls_B:
	ds_read_b128 v[102:105], v186
	ds_read_b128 v[106:109], v186 offset:9216
	ds_read_b128 v[110:113], v186 offset:32
	ds_read_b128 v[86:89], v186 offset:9248
	ds_read_b128 v[90:93], v186 offset:64
	ds_read_b128 v[172:175], v186 offset:9280
	ds_read_b128 v[72:75], v186 offset:96
	v_max3_f32 v76, v146, v147, v148
	v_max3_f32 v77, v34, v35, v36
	v_max3_f32 v76, v76, v149, v150
	v_max3_f32 v77, v77, v37, v38
	v_max3_f32 v76, v76, v151, v152
	v_max3_f32 v77, v77, v39, v40
	v_max3_f32 v76, v76, v153, v154
	v_max3_f32 v77, v77, v41, v42
	v_max3_f32 v76, v76, v155, v156
	v_max3_f32 v77, v77, v43, v44
	v_max3_f32 v76, v76, v157, v158
	v_max3_f32 v77, v77, v45, v46
	v_max3_f32 v76, v76, v159, v160
	v_max3_f32 v77, v77, v47, v48
	v_max_f32_e32 v76, v76, v161
	v_max_f32_e32 v77, v77, v49
	v_max_f32_e32 v85, v84, v76
	v_sub_f32_e32 v76, v84, v85
	v_exp_f32_e32 v76, v76
	v_mov_b32_e32 v84, v85
	v_sub_f32_e32 v146, v146, v85
	v_sub_f32_e32 v147, v147, v85
	v_sub_f32_e32 v148, v148, v85
	v_sub_f32_e32 v149, v149, v85
	v_sub_f32_e32 v150, v150, v85
	v_sub_f32_e32 v151, v151, v85
	v_sub_f32_e32 v152, v152, v85
	v_sub_f32_e32 v153, v153, v85
	v_sub_f32_e32 v154, v154, v85
	v_sub_f32_e32 v155, v155, v85
	v_sub_f32_e32 v156, v156, v85
	v_sub_f32_e32 v157, v157, v85
	v_sub_f32_e32 v158, v158, v85
	v_sub_f32_e32 v159, v159, v85
	v_sub_f32_e32 v160, v160, v85
	v_sub_f32_e32 v161, v161, v85
	v_max_f32_e32 v85, v83, v77
	v_sub_f32_e32 v77, v83, v85
	v_exp_f32_e32 v77, v77
	v_mov_b32_e32 v83, v85
	v_sub_f32_e32 v34, v34, v85
	v_sub_f32_e32 v35, v35, v85
	v_sub_f32_e32 v36, v36, v85
	v_sub_f32_e32 v37, v37, v85
	v_sub_f32_e32 v38, v38, v85
	v_sub_f32_e32 v39, v39, v85
	v_sub_f32_e32 v40, v40, v85
	v_sub_f32_e32 v41, v41, v85
	v_sub_f32_e32 v42, v42, v85
	v_sub_f32_e32 v43, v43, v85
	v_sub_f32_e32 v44, v44, v85
	v_sub_f32_e32 v45, v45, v85
	v_sub_f32_e32 v46, v46, v85
	v_sub_f32_e32 v47, v47, v85
	v_sub_f32_e32 v48, v48, v85
	v_sub_f32_e32 v49, v49, v85
	v_exp_f32_e32 v146, v146
	v_exp_f32_e32 v34, v34
	s_waitcnt lgkmcnt(6)
	v_mfma_f32_32x32x16_f16 v[2:17], v[102:105], v[114:117], 0
	v_exp_f32_e32 v147, v147
	v_exp_f32_e32 v35, v35
	v_exp_f32_e32 v148, v148
	v_exp_f32_e32 v36, v36
	s_waitcnt lgkmcnt(5)
	v_mfma_f32_32x32x16_f16 v[18:33], v[106:109], v[130:133], 0
	v_exp_f32_e32 v149, v149
	v_exp_f32_e32 v37, v37
	v_exp_f32_e32 v150, v150
	v_exp_f32_e32 v38, v38
	s_waitcnt lgkmcnt(4)
	v_mfma_f32_32x32x16_f16 v[2:17], v[110:113], v[118:121], v[2:17]
	v_exp_f32_e32 v151, v151
	v_exp_f32_e32 v39, v39
	v_exp_f32_e32 v152, v152
	v_exp_f32_e32 v40, v40
	s_waitcnt lgkmcnt(3)
	v_mfma_f32_32x32x16_f16 v[18:33], v[86:89], v[134:137], v[18:33]
	v_exp_f32_e32 v153, v153
	v_exp_f32_e32 v41, v41
	s_waitcnt vmcnt(0)
	ds_write_b128 v185, v[50:53] offset:18432
	ds_write_b128 v185, v[94:97] offset:27648
	ds_read_b128 v[50:53], v186 offset:9312
	s_min_u32 s12, s0, 27
	s_add_i32 s12, s18, s12
	s_lshl_b32 s12, s12, 13
	s_and_b32 s12, s12, 0x3e000
	s_add_u32 s28, s12, s3
	s_mov_b32 s29, 0
	v_lshl_add_u64 v[176:177], v[170:171], 0, s[12:13]
	global_load_dwordx4 v[162:165], v[176:177], off
	v_lshl_add_u64 v[176:177], v[170:171], 0, s[28:29]
	global_load_dwordx4 v[166:169], v[176:177], off
	v_exp_f32_e32 v154, v154
	v_exp_f32_e32 v42, v42
	v_exp_f32_e32 v155, v155
	v_exp_f32_e32 v43, v43
	s_waitcnt lgkmcnt(5)
	v_mfma_f32_32x32x16_f16 v[2:17], v[90:93], v[122:125], v[2:17]
	v_exp_f32_e32 v156, v156
	v_exp_f32_e32 v44, v44
	v_exp_f32_e32 v157, v157
	v_exp_f32_e32 v45, v45
	s_waitcnt lgkmcnt(4)
	v_mfma_f32_32x32x16_f16 v[18:33], v[172:175], v[138:141], v[18:33]
	v_exp_f32_e32 v158, v158
	v_exp_f32_e32 v46, v46
	v_exp_f32_e32 v159, v159
	v_exp_f32_e32 v47, v47
	s_waitcnt lgkmcnt(3)
	v_mfma_f32_32x32x16_f16 v[2:17], v[72:75], v[126:129], v[2:17]
	v_exp_f32_e32 v160, v160
	v_exp_f32_e32 v48, v48
	v_exp_f32_e32 v161, v161
	v_exp_f32_e32 v49, v49
	v_add_f32_e32 v146, v146, v147
	v_add_f32_e32 v148, v148, v149
	v_add_f32_e32 v150, v150, v151
	v_add_f32_e32 v152, v152, v153
	v_add_f32_e32 v154, v154, v155
	v_add_f32_e32 v156, v156, v157
	v_add_f32_e32 v158, v158, v159
	v_add_f32_e32 v160, v160, v161
	v_add_f32_e32 v34, v34, v35
	v_add_f32_e32 v36, v36, v37
	s_waitcnt lgkmcnt(0)
	v_mfma_f32_32x32x16_f16 v[18:33], v[50:53], v[142:145], v[18:33]
	v_add_f32_e32 v38, v38, v39
	v_add_f32_e32 v40, v40, v41
	v_add_f32_e32 v42, v42, v43
	v_add_f32_e32 v44, v44, v45
	v_add_f32_e32 v46, v46, v47
	v_add_f32_e32 v48, v48, v49
	v_add_f32_e32 v146, v146, v148
	v_add_f32_e32 v150, v150, v152
	v_add_f32_e32 v154, v154, v156
	v_add_f32_e32 v158, v158, v160
	v_add_f32_e32 v34, v34, v36
	v_add_f32_e32 v38, v38, v40
	v_add_f32_e32 v42, v42, v44
	v_add_f32_e32 v46, v46, v48
	v_add_f32_e32 v146, v146, v150
	v_add_f32_e32 v154, v154, v158
	v_add_f32_e32 v34, v34, v38
	v_add_f32_e32 v42, v42, v46
	v_add_f32_e32 v146, v146, v154
	v_add_f32_e32 v34, v34, v42
	v_fma_f32 v63, v63, v76, v146
	v_fma_f32 v62, v62, v77, v34
	s_waitcnt lgkmcnt(0)
	s_barrier
	s_cmp_lt_u32 s0, 30
	s_cbranch_scc1 .Ls_A
.Ll1_done:
	s_waitcnt vmcnt(0)
	s_cmp_eq_u32 s37, 1
	s_cbranch_scc1 .Ll1_cont
	v_cmp_gt_f32_e64 vcc, v63, s26
	v_cmp_gt_f32_e64 s[28:29], v62, s26
	s_or_b64 vcc, vcc, s[28:29]
	v_cmp_lt_f32_e64 s[28:29], v63, s27
	s_or_b64 vcc, vcc, s[28:29]
	v_cmp_lt_f32_e64 s[28:29], v62, s27
	s_or_b64 vcc, vcc, s[28:29]
	s_cbranch_vccz .Ll1_noflag
	v_mov_b32_e32 v85, 0x12000
	v_mov_b32_e32 v86, 1
	ds_write_b32 v85, v86
.Ll1_noflag:
	s_waitcnt lgkmcnt(0)
	s_barrier
	v_mov_b32_e32 v85, 0x12000
	ds_read_b32 v86, v85
	s_waitcnt lgkmcnt(0)
	v_readfirstlane_b32 s28, v86
	s_cmp_eq_u32 s28, 0
	s_cbranch_scc1 .Ll1_cont
	s_mov_b32 s37, 1
	s_mov_b32 s0, s32
	s_mov_b32 s1, s33
	s_mov_b32 s3, s34
	s_mov_b32 s4, s35
	s_mov_b32 s5, s36
	v_mov_b32_e32 v63, 0
	v_lshrrev_b32_e32 v2, 1, v0
	s_branch .Lp_top
.Ll1_cont:
	ds_bpermute_b32 v2, v69, v84
	ds_bpermute_b32 v5, v69, v83
	v_max_f32_e32 v4, v84, v84
	v_max_f32_e32 v7, v83, v83
	ds_bpermute_b32 v3, v69, v63
	s_waitcnt lgkmcnt(2)
	v_max_f32_e32 v6, v2, v2
	v_max_f32_e32 v4, v4, v6
	v_sub_f32_e32 v6, v84, v4
	v_exp_f32_e32 v9, v6
	s_waitcnt lgkmcnt(1)
	v_max_f32_e32 v6, v5, v5
	v_sub_f32_e32 v2, v2, v4
	v_max_f32_e32 v6, v7, v6
	v_exp_f32_e32 v11, v2
	ds_bpermute_b32 v2, v69, v62
	v_sub_f32_e32 v5, v5, v6
	v_sub_f32_e32 v7, v83, v6
	v_exp_f32_e32 v10, v5
	v_exp_f32_e32 v8, v7
	v_cmp_gt_u32_e32 vcc, 32, v98
	s_waitcnt lgkmcnt(0)
	v_pk_mul_f32 v[2:3], v[10:11], v[2:3]
	s_nop 0
	v_pk_fma_f32 v[8:9], v[62:63], v[8:9], v[2:3]
	v_lshlrev_b32_e32 v2, 7, v184
	v_or3_b32 v10, v183, v2, v1
	s_and_saveexec_b64 s[0:1], vcc
	v_lshl_add_u32 v2, v10, 4, 0
	v_add_u32_e32 v2, 0x21000, v2
	v_mov_b32_e32 v5, v9
	v_mov_b32_e32 v7, v8
	ds_write_b128 v2, v[4:7]
	s_or_b64 exec, exec, s[0:1]
	s_lshl_b32 s12, s21, 7
	s_mov_b32 s3, 0
	v_or_b32_e32 v2, s12, v82
	s_lshl_b32 s13, s21, 11
	s_add_i32 s23, 0, 0x12000
	v_lshlrev_b32_e32 v2, 12, v2
	v_mov_b32_e32 v3, 0
	s_add_i32 s13, s13, s16
	s_lshl_b64 s[0:1], s[2:3], 13
	v_lshl_add_u64 v[12:13], s[14:15], 0, v[2:3]
	v_mov_b32_e32 v69, v3
	s_add_u32 s0, s10, s0
	v_lshl_add_u64 v[172:173], v[12:13], 0, v[68:69]
	s_addc_u32 s1, s11, s1
	s_lshl_b32 s10, s22, 7
	s_mov_b32 s11, s3
	s_waitcnt vmcnt(1)
	v_lshl_add_u64 v[36:37], v[172:173], 0, s[10:11]
	s_mov_b32 s10, 0x40000
	v_add_co_u32_e32 v38, vcc, s10, v36
	s_waitcnt lgkmcnt(0)
	s_barrier
	global_load_dwordx4 v[12:15], v[58:59], off
	global_load_dwordx4 v[16:19], v[70:71], off
	v_addc_co_u32_e32 v39, vcc, 0, v37, vcc
	global_load_dwordx4 v[20:23], v[56:57], off
	global_load_dwordx4 v[24:27], v[66:67], off
	global_load_dwordx4 v[28:31], v[36:37], off
	global_load_dwordx4 v[32:35], v[38:39], off
	v_add_f32_e32 v2, v78, v80
	s_movk_i32 s11, 0x1200
	v_add_f32_e32 v5, v79, v81
	s_mov_b32 s14, 0x3fb8aa3b
	v_lshlrev_b32_e32 v10, 4, v10
	v_mov_b32_e32 v36, s23
	v_mul_f32_e32 v37, 0x3fb8aa3b, v2
	v_mul_f32_e32 v38, 0x3fb8aa3b, v5
	v_xor_b32_e32 v10, 0x800, v10
	v_mad_u32_u24 v40, v55, s11, v36
	v_fma_f32 v36, v2, s14, -v37
	v_rndne_f32_e32 v39, v37
	v_fma_f32 v41, v5, s14, -v38
	s_waitcnt vmcnt(6)
	v_rndne_f32_e32 v42, v38
	v_add_u32_e32 v10, 0, v10
	v_fmac_f32_e32 v36, 0x32a5705f, v2
	v_sub_f32_e32 v37, v37, v39
	v_fmac_f32_e32 v41, 0x32a5705f, v5
	v_sub_f32_e32 v38, v38, v42
	v_add_u32_e32 v10, 0x21000, v10
	v_add_f32_e32 v44, v37, v36
	global_load_dwordx4 v[146:149], v[60:61], off
	global_load_dwordx4 v[150:153], v[64:65], off
	v_cvt_i32_f32_e32 v43, v39
	v_add_f32_e32 v41, v38, v41
	ds_read_b128 v[36:39], v10
	v_exp_f32_e32 v10, v44
	v_cvt_i32_f32_e32 v42, v42
	v_exp_f32_e32 v41, v41
	s_mov_b32 s21, 0xc2ce8ed0
	s_lshl_b32 s11, s20, 6
	s_add_i32 s14, s11, 64
	v_ldexp_f32 v10, v10, v43
	v_cmp_ngt_f32_e32 vcc, s21, v2
	s_mov_b32 s22, 0x42b17218
	s_and_b32 s14, s14, 0x7c0
	v_ldexp_f32 v41, v41, v42
	v_cndmask_b32_e32 v10, 0, v10, vcc
	v_cmp_ngt_f32_e32 vcc, s21, v5
	v_mov_b32_e32 v7, 0x7f800000
	v_max_f32_e32 v11, v4, v4
	s_mov_b32 s15, s3
	s_lshl_b32 s14, s14, 1
	s_waitcnt lgkmcnt(0)
	v_max_f32_e32 v42, v36, v36
	v_cndmask_b32_e32 v41, 0, v41, vcc
	v_cmp_nlt_f32_e32 vcc, s22, v2
	v_max_f32_e32 v187, v11, v42
	v_mov_b32_e32 v55, v3
	v_cndmask_b32_e32 v2, v7, v10, vcc
	v_cmp_nlt_f32_e32 vcc, s22, v5
	v_lshl_add_u64 v[10:11], v[172:173], 0, s[14:15]
	v_lshl_add_u64 v[178:179], s[0:1], 0, v[54:55]
	v_cndmask_b32_e32 v5, v7, v41, vcc
	v_sub_f32_e32 v2, v2, v5
	v_add_f32_e32 v41, 0x3e4ccccd, v2
	v_sub_f32_e32 v2, v4, v187
	v_max_f32_e32 v4, v6, v6
	s_and_b32 s1, s2, 7
	s_mulk_i32 s1, 0x280
	s_mulk_i32 s19, 0x140
	s_add_i32 s0, s20, 2
	s_waitcnt vmcnt(7)
	ds_write_b128 v185, v[12:15]
	s_waitcnt vmcnt(6)
	ds_write_b128 v185, v[16:19] offset:9216
	s_waitcnt vmcnt(5)
	ds_write_b128 v185, v[20:23] offset:18432
	s_waitcnt vmcnt(4)
	ds_write_b128 v185, v[24:27] offset:27648
	s_waitcnt vmcnt(3)
	ds_write_b128 v185, v[28:31] offset:36864
	s_waitcnt vmcnt(2)
	ds_write_b128 v185, v[32:35] offset:46080
	v_add_co_u32_e32 v12, vcc, s10, v10
	v_exp_f32_e32 v23, v2
	s_nop 0
	v_addc_co_u32_e32 v13, vcc, 0, v11, vcc
	global_load_dwordx4 v[154:157], v[10:11], off
	global_load_dwordx4 v[158:161], v[12:13], off
	s_waitcnt lgkmcnt(0)
	s_barrier
	ds_read_b128 v[10:13], v186
	v_sub_f32_e32 v2, v36, v187
	v_exp_f32_e32 v25, v2
	v_max_f32_e32 v2, v38, v38
	v_max_f32_e32 v188, v4, v2
	v_sub_f32_e32 v2, v6, v188
	v_exp_f32_e32 v22, v2
	v_sub_f32_e32 v2, v38, v188
	v_exp_f32_e32 v24, v2
	ds_read_b128 v[14:17], v186 offset:9216
	ds_read_b128 v[18:21], v186 offset:32
	s_waitcnt lgkmcnt(2)
	v_mfma_f32_32x32x16_f16 v[66:81], v[10:13], v[114:117], 0
	v_mov_b32_e32 v36, v39
	v_mul_f32_e64 v10, v36, v24
	v_mul_f32_e64 v11, v37, v25
	ds_read_b128 v[4:7], v186 offset:9248
	s_add_i32 s1, s1, s19
	s_mov_b32 s14, 0x30000
	s_mov_b32 s15, 0x80000
	s_mov_b32 s19, 0
	s_waitcnt lgkmcnt(2)
	v_mfma_f32_32x32x16_f16 v[82:97], v[14:17], v[130:133], 0
	v_fma_f32 v16, v8, v22, v10
	v_fma_f32 v17, v9, v23, v11
	v_log_f32_e32 v238, v17
	s_nop 0
	v_add_f32_e32 v187, v187, v238
	v_sub_f32_e32 v240, 0, v187
	v_sub_f32_e32 v241, 0, v187
	v_sub_f32_e32 v242, 0, v187
	v_sub_f32_e32 v243, 0, v187
	v_sub_f32_e32 v244, 0, v187
	v_sub_f32_e32 v245, 0, v187
	v_sub_f32_e32 v246, 0, v187
	v_sub_f32_e32 v247, 0, v187
	v_sub_f32_e32 v248, 0, v187
	v_sub_f32_e32 v249, 0, v187
	v_sub_f32_e32 v250, 0, v187
	v_sub_f32_e32 v251, 0, v187
	v_sub_f32_e32 v252, 0, v187
	v_sub_f32_e32 v253, 0, v187
	v_sub_f32_e32 v254, 0, v187
	v_sub_f32_e32 v255, 0, v187
	v_lshrrev_b32_e32 v22, 3, v98
	v_or3_b32 v2, s13, v183, v22
	v_lshlrev_b64 v[8:9], 13, v[2:3]
	v_lshl_add_u64 v[8:9], s[4:5], 0, v[8:9]
	v_lshlrev_b32_e32 v2, 2, v101
	v_lshl_add_u64 v[8:9], v[8:9], 0, v[2:3]
	v_and_b32_e32 v2, 0x70, v54
	v_lshl_add_u64 v[174:175], v[8:9], 0, v[2:3]
	ds_read_b128 v[8:11], v186 offset:64
	s_waitcnt lgkmcnt(2)
	v_mfma_f32_32x32x16_f16 v[66:81], v[18:21], v[118:121], v[66:81]
	v_div_scale_f32 v18, s[4:5], v16, v16, -v41
	v_rcp_f32_e32 v19, v18
	v_div_scale_f32 v20, vcc, -v41, v16, -v41
	s_mov_b32 s13, 0x20000
	v_mov_b32_e32 v24, v3
	s_waitcnt lgkmcnt(1)
	v_mfma_f32_32x32x16_f16 v[82:97], v[4:7], v[134:137], v[82:97]
	v_fma_f32 v4, -v18, v19, 1.0
	v_fmac_f32_e32 v19, v4, v19
	v_mul_f32_e32 v21, v20, v19
	ds_read_b128 v[4:7], v186 offset:9280
	ds_read_b128 v[12:15], v186 offset:96
	v_mov_b32_e32 v25, v3
	v_mov_b32_e32 v26, v3
	v_mov_b32_e32 v27, v3
	s_waitcnt lgkmcnt(2)
	v_mfma_f32_32x32x16_f16 v[66:81], v[8:11], v[122:125], v[66:81]
	v_fma_f32 v8, -v18, v21, v20
	v_fmac_f32_e32 v21, v8, v19
	v_fma_f32 v18, -v18, v21, v20
	v_div_scale_f32 v20, s[4:5], v17, v17, 1.0
	v_rcp_f32_e32 v23, v20
	ds_read_b128 v[8:11], v186 offset:9312
	s_waitcnt lgkmcnt(2)
	v_mfma_f32_32x32x16_f16 v[82:97], v[4:7], v[138:141], v[82:97]
	v_div_fmas_f32 v4, v18, v19, v21
	v_div_fixup_f32 v176, v4, v16, -v41
	v_fma_f32 v4, -v20, v23, 1.0
	v_fmac_f32_e32 v23, v4, v23
	v_div_scale_f32 v4, vcc, 1.0, v17, 1.0
	v_mul_f32_e32 v5, v4, v23
	v_fma_f32 v6, -v20, v5, v4
	v_fmac_f32_e32 v5, v6, v23
	s_waitcnt lgkmcnt(1)
	v_mfma_f32_32x32x16_f16 v[66:81], v[12:15], v[126:129], v[66:81]
	v_fma_f32 v4, -v20, v5, v4
	v_div_fmas_f32 v4, v4, v23, v5
	v_div_fixup_f32 v177, v4, v17, 1.0
	v_mul_u32_u24_e32 v4, 0x90, v22
	v_add3_u32 v189, v40, v4, v2
	v_mul_u32_u24_e32 v2, 0x90, v1
	v_lshlrev_b32_e32 v4, 2, v99
	s_waitcnt lgkmcnt(0)
	v_mfma_f32_32x32x16_f16 v[82:97], v[8:11], v[142:145], v[82:97]
	v_add3_u32 v190, v40, v2, v4
	v_mul_u32_u24_e32 v2, 0x48, v1
	v_lshl_add_u32 v2, v2, 1, 0
	v_lshlrev_b32_e32 v4, 1, v101
	v_add3_u32 v191, v2, v4, v100
	s_mov_b32 s4, 0x3f800000
	s_mov_b32 s5, 0x10000
	v_mov_b32_e32 v2, v3
	v_mov_b32_e32 v4, v3
	v_mov_b32_e32 v5, v3
	v_mov_b32_e32 v6, v3
	v_mov_b32_e32 v7, v3
	v_mov_b32_e32 v8, v3
	v_mov_b32_e32 v9, v3
	v_mov_b32_e32 v10, v3
	v_mov_b32_e32 v11, v3
	v_mov_b32_e32 v12, v3
	v_mov_b32_e32 v13, v3
	v_mov_b32_e32 v14, v3
	v_mov_b32_e32 v15, v3
	v_mov_b32_e32 v16, v3
	v_mov_b32_e32 v17, v3
	v_mov_b32_e32 v18, v3
	v_mov_b32_e32 v19, v3
	v_mov_b32_e32 v20, v3
	v_mov_b32_e32 v21, v3
	v_mov_b32_e32 v22, v3
	v_mov_b32_e32 v23, v3
	v_mov_b32_e32 v28, v3
	v_mov_b32_e32 v29, v3
	v_mov_b32_e32 v30, v3
	v_mov_b32_e32 v31, v3
	v_mov_b32_e32 v32, v3
	v_mov_b32_e32 v33, v3
	v_mov_b32_e32 v34, v3
	v_mov_b32_e32 v35, v3
	v_mov_b32_e32 v36, v3
	v_mov_b32_e32 v37, v3
	v_mov_b32_e32 v38, v3
	v_mov_b32_e32 v39, v3
	v_mov_b32_e32 v40, v3
	v_mov_b32_e32 v41, v3
	v_mov_b32_e32 v42, v3
	v_mov_b32_e32 v43, v3
	v_mov_b32_e32 v44, v3
	v_mov_b32_e32 v45, v3
	v_mov_b32_e32 v46, v3
	v_mov_b32_e32 v47, v3
	v_mov_b32_e32 v48, v3
	v_mov_b32_e32 v49, v3
	v_mov_b32_e32 v50, v3
	v_mov_b32_e32 v51, v3
	v_mov_b32_e32 v52, v3
	v_mov_b32_e32 v53, v3
	v_mov_b32_e32 v54, v3
	v_mov_b32_e32 v56, v3
	v_mov_b32_e32 v57, v3
	v_mov_b32_e32 v58, v3
	v_mov_b32_e32 v59, v3
	v_mov_b32_e32 v60, v3
	v_mov_b32_e32 v61, v3
	v_mov_b32_e32 v62, v3
	v_mov_b32_e32 v63, v3
	v_mov_b32_e32 v64, v3
	v_mov_b32_e32 v65, v3
	v_add_u32_e32 v192, 0xd800, v191
	v_sub_f32_e32 v66, v66, v187
	v_sub_f32_e32 v67, v67, v187
	v_sub_f32_e32 v68, v68, v187
	v_sub_f32_e32 v69, v69, v187
	v_sub_f32_e32 v70, v70, v187
	v_sub_f32_e32 v71, v71, v187
	v_sub_f32_e32 v72, v72, v187
	v_sub_f32_e32 v73, v73, v187
	v_sub_f32_e32 v74, v74, v187
	v_sub_f32_e32 v75, v75, v187
	v_sub_f32_e32 v76, v76, v187
	v_sub_f32_e32 v77, v77, v187
	v_sub_f32_e32 v78, v78, v187
	v_sub_f32_e32 v79, v79, v187
	v_sub_f32_e32 v80, v80, v187
	v_sub_f32_e32 v81, v81, v187
	s_mov_b32 s27, 0x42c80000
	v_cmp_gt_f32_e64 vcc, |v188|, s27
	s_cbranch_vccnz .Ll2_gen
	v_sub_f32_e32 v238, 0, v188
	v_exp_f32_e32 v238, v238
	s_nop 0
	v_mul_f32_e32 v176, v176, v238
	s_barrier
	s_branch .Ll2f_top
.Ll2_gen:
	s_barrier
.LBB4_7:
	v_exp_f32_e32 v215, v66
	s_nop 7
	v_fma_f32 v66, v82, s4, -v188
	v_exp_f32_e32 v216, v66
	v_exp_f32_e32 v217, v67
	v_fma_f32 v66, v83, s4, -v188
	v_exp_f32_e32 v214, v66
	v_exp_f32_e32 v219, v68
	v_fma_f32 v66, v84, s4, -v188
	v_exp_f32_e32 v220, v66
	ds_read_b128 v[98:101], v186 offset:18432
	ds_read_b128 v[162:165], v186 offset:18464
	ds_read_b128 v[194:197], v186 offset:27648
	ds_read_b128 v[198:201], v186 offset:27680
	ds_read_b128 v[202:205], v186 offset:18496
	ds_read_b128 v[206:209], v186 offset:18528
	ds_read_b128 v[210:213], v186 offset:27712
	ds_read_b128 v[166:169], v186 offset:27744
	v_exp_f32_e32 v221, v69
	v_fma_f32 v66, v85, s4, -v188
	v_exp_f32_e32 v218, v66
	s_waitcnt lgkmcnt(7)
	v_mfma_f32_32x32x16_f16 v[98:113], v[98:101], v[114:117], v[240:255]
	v_exp_f32_e32 v223, v70
	v_fma_f32 v66, v86, s4, -v188
	v_exp_f32_e32 v70, v66
	v_exp_f32_e32 v71, v71
	v_fma_f32 v66, v87, s4, -v188
	v_exp_f32_e32 v222, v66
	v_exp_f32_e32 v225, v72
	v_fma_f32 v66, v88, s4, -v188
	v_exp_f32_e32 v226, v66
	v_exp_f32_e32 v227, v73
	v_fma_f32 v66, v89, s4, -v188
	v_exp_f32_e32 v224, v66
	s_waitcnt lgkmcnt(6)
	v_mfma_f32_32x32x16_f16 v[98:113], v[162:165], v[118:121], v[98:113]
	v_exp_f32_e32 v229, v74
	v_fma_f32 v66, v90, s4, -v188
	v_exp_f32_e32 v230, v66
	v_exp_f32_e32 v231, v75
	v_fma_f32 v66, v91, s4, -v188
	v_exp_f32_e32 v228, v66
	v_exp_f32_e32 v233, v76
	v_fma_f32 v66, v92, s4, -v188
	v_exp_f32_e32 v234, v66
	v_exp_f32_e32 v235, v77
	v_fma_f32 v66, v93, s4, -v188
	v_exp_f32_e32 v232, v66
	s_waitcnt lgkmcnt(3)
	v_mfma_f32_32x32x16_f16 v[98:113], v[202:205], v[122:125], v[98:113]
	v_exp_f32_e32 v237, v78
	v_fma_f32 v66, v94, s4, -v188
	v_exp_f32_e32 v162, v66
	v_exp_f32_e32 v163, v79
	v_fma_f32 v66, v95, s4, -v188
	v_exp_f32_e32 v236, v66
	v_exp_f32_e32 v165, v80
	v_fma_f32 v66, v96, s4, -v188
	v_exp_f32_e32 v202, v66
	v_exp_f32_e32 v203, v81
	v_fma_f32 v66, v97, s4, -v188
	v_exp_f32_e32 v193, v66
	s_waitcnt lgkmcnt(2)
	v_mfma_f32_32x32x16_f16 v[98:113], v[206:209], v[126:129], v[98:113]
	s_waitcnt vmcnt(3)
	ds_write_b128 v185, v[146:149]
	s_waitcnt vmcnt(2)
	ds_write_b128 v185, v[150:153] offset:9216
	s_waitcnt vmcnt(1)
	ds_write_b128 v185, v[154:157] offset:55296
	s_waitcnt vmcnt(0)
	ds_write_b128 v185, v[158:161] offset:64512
	v_fma_f32 v150, v176, v216, v215
	v_fma_f32 v151, v176, v214, v217
	ds_read_b128 v[66:69], v189
	ds_read_b128 v[88:91], v189 offset:1152
	v_fma_f32 v152, v176, v220, v219
	v_fma_f32 v153, v176, v218, v221
	ds_read_b128 v[92:95], v189 offset:2304
	ds_read_b128 v[146:149], v189 offset:3456
	v_fma_f32 v154, v176, v70, v223
	v_fma_f32 v155, v176, v222, v71
	ds_write_b128 v190, v[150:153]
	v_fma_f32 v156, v176, v226, v225
	v_fma_f32 v157, v176, v224, v227
	ds_write_b128 v190, v[154:157] offset:16
	v_fma_f32 v158, v176, v230, v229
	v_fma_f32 v159, v176, v228, v231
	v_cvt_pk_f16_f32 v157, v156, v157
	v_fma_f32 v160, v176, v234, v233
	v_fma_f32 v161, v176, v232, v235
	ds_write_b128 v190, v[158:161] offset:64
	v_fma_f32 v162, v176, v162, v237
	v_fma_f32 v163, v176, v236, v163
	v_cvt_pk_f16_f32 v156, v154, v155
	v_fma_f32 v164, v176, v202, v165
	v_fma_f32 v165, v176, v193, v203
	ds_write_b128 v190, v[162:165] offset:80
	v_cvt_pk_f16_f32 v155, v152, v153
	v_cvt_pk_f16_f32 v154, v150, v151
	ds_read_b128 v[150:153], v191 offset:36864
	s_cmp_eq_u32 s19, 0
	s_cselect_b64 vcc, -1, 0
	s_add_i32 s20, s16, s1
	v_mfma_f32_32x32x16_f16 v[72:87], v[194:197], v[130:133], 0
	ds_read_b128 v[194:197], v191 offset:36896
	s_add_i32 s2, s20, 0x7c0
	s_and_b32 s2, s2, 0x7c0
	s_lshl_b32 s2, s2, 2
	v_lshl_add_u64 v[70:71], v[174:175], 0, s[2:3]
	v_cndmask_b32_e32 v71, v71, v179, vcc
	v_cndmask_b32_e32 v70, v70, v178, vcc
	s_waitcnt lgkmcnt(1)
	v_mfma_f32_32x32x16_f16 v[50:65], v[154:157], v[150:153], v[50:65]
	ds_read_b128 v[150:153], v191 offset:41472
	global_store_dwordx4 v[70:71], v[66:69], off nt
	ds_read_b128 v[66:69], v191 offset:41504
	v_cvt_pk_f16_f32 v165, v164, v165
	v_cvt_pk_f16_f32 v164, v162, v163
	v_cvt_pk_f16_f32 v163, v160, v161
	v_cvt_pk_f16_f32 v162, v158, v159
	s_waitcnt lgkmcnt(1)
	v_mfma_f32_32x32x16_f16 v[34:49], v[154:157], v[150:153], v[34:49]
	v_add_co_u32_e32 v96, vcc, s5, v70
	s_min_u32 s2, s19, 28
	s_nop 0
	v_addc_co_u32_e32 v97, vcc, 0, v71, vcc
	global_store_dwordx4 v[96:97], v[88:91], off nt
	s_add_i32 s21, s17, s2
	s_waitcnt lgkmcnt(0)
	v_mfma_f32_32x32x16_f16 v[34:49], v[162:165], v[66:69], v[34:49]
	ds_read_b128 v[66:69], v191 offset:46080
	v_add_co_u32_e32 v88, vcc, s13, v70
	s_lshl_b32 s2, s21, 13
	s_nop 0
	v_addc_co_u32_e32 v89, vcc, 0, v71, vcc
	global_store_dwordx4 v[88:89], v[92:95], off nt
	ds_read_b128 v[88:91], v191 offset:46112
	s_waitcnt lgkmcnt(1)
	v_mfma_f32_32x32x16_f16 v[18:33], v[154:157], v[66:69], v[18:33]
	v_add_co_u32_e32 v70, vcc, s14, v70
	s_and_b32 s2, s2, 0x3e000
	s_nop 0
	v_addc_co_u32_e32 v71, vcc, 0, v71, vcc
	v_lshl_add_u64 v[66:67], v[170:171], 0, s[2:3]
	v_add_co_u32_e32 v68, vcc, s15, v66
	global_store_dwordx4 v[70:71], v[146:149], off nt
	s_nop 0
	v_addc_co_u32_e32 v69, vcc, 0, v67, vcc
	s_waitcnt lgkmcnt(0)
	v_mfma_f32_32x32x16_f16 v[18:33], v[162:165], v[88:91], v[18:33]
	global_load_dwordx4 v[88:91], v[66:67], off
	global_load_dwordx4 v[92:95], v[68:69], off
	ds_read_b128 v[66:69], v191 offset:50688
	ds_read_b128 v[146:149], v191 offset:50720
	s_min_u32 s2, s19, 29
	s_add_i32 s2, s0, s2
	s_lshl_b32 s2, s2, 7
	s_and_b32 s2, s2, 0xf80
	s_waitcnt lgkmcnt(1)
	v_mfma_f32_32x32x16_f16 v[2:17], v[154:157], v[66:69], v[2:17]
	v_lshl_add_u64 v[66:67], v[172:173], 0, s[2:3]
	v_add_co_u32_e32 v68, vcc, s10, v66
	s_nop 0
	v_addc_co_u32_e32 v69, vcc, 0, v67, vcc
	global_load_dwordx4 v[150:153], v[66:67], off
	global_load_dwordx4 v[154:157], v[68:69], off
	v_mfma_f32_32x32x16_f16 v[72:87], v[198:201], v[134:137], v[72:87]
	v_exp_f32_e32 v97, v98
	s_waitcnt lgkmcnt(0)
	s_barrier
	v_mfma_f32_32x32x16_f16 v[72:87], v[210:213], v[138:141], v[72:87]
	v_mfma_f32_32x32x16_f16 v[72:87], v[166:169], v[142:145], v[72:87]
	v_mfma_f32_32x32x16_f16 v[50:65], v[162:165], v[194:197], v[50:65]
	s_nop 10
	v_fma_f32 v70, v72, s4, -v188
	v_exp_f32_e32 v166, v70
	v_exp_f32_e32 v167, v99
	v_fma_f32 v70, v73, s4, -v188
	v_exp_f32_e32 v96, v70
	v_exp_f32_e32 v99, v100
	v_fma_f32 v70, v74, s4, -v188
	v_exp_f32_e32 v168, v70
	v_exp_f32_e32 v169, v101
	v_fma_f32 v70, v75, s4, -v188
	v_exp_f32_e32 v98, v70
	v_exp_f32_e32 v101, v102
	v_fma_f32 v70, v76, s4, -v188
	v_exp_f32_e32 v210, v70
	v_exp_f32_e32 v211, v103
	v_fma_f32 v70, v77, s4, -v188
	v_exp_f32_e32 v100, v70
	v_exp_f32_e32 v103, v104
	v_fma_f32 v70, v78, s4, -v188
	v_exp_f32_e32 v212, v70
	v_exp_f32_e32 v213, v105
	v_fma_f32 v70, v79, s4, -v188
	v_exp_f32_e32 v102, v70
	v_exp_f32_e32 v105, v106
	v_fma_f32 v70, v80, s4, -v188
	v_exp_f32_e32 v214, v70
	v_exp_f32_e32 v215, v107
	v_fma_f32 v70, v81, s4, -v188
	v_mfma_f32_32x32x16_f16 v[2:17], v[162:165], v[146:149], v[2:17]
	ds_read_b128 v[66:69], v186
	ds_read_b128 v[158:161], v186 offset:32
	ds_read_b128 v[194:197], v186 offset:9216
	ds_read_b128 v[198:201], v186 offset:9248
	ds_read_b128 v[202:205], v186 offset:64
	ds_read_b128 v[206:209], v186 offset:96
	ds_read_b128 v[146:149], v186 offset:9280
	ds_read_b128 v[162:165], v186 offset:9312
	v_exp_f32_e32 v104, v70
	v_exp_f32_e32 v107, v108
	v_fma_f32 v82, v82, s4, -v188
	v_exp_f32_e32 v216, v82
	s_waitcnt lgkmcnt(7)
	v_mfma_f32_32x32x16_f16 v[66:81], v[66:69], v[114:117], v[240:255]
	v_exp_f32_e32 v217, v109
	v_fma_f32 v82, v83, s4, -v188
	v_exp_f32_e32 v106, v82
	v_exp_f32_e32 v109, v110
	v_fma_f32 v82, v84, s4, -v188
	v_exp_f32_e32 v218, v82
	s_waitcnt lgkmcnt(6)
	v_mfma_f32_32x32x16_f16 v[66:81], v[158:161], v[118:121], v[66:81]
	v_exp_f32_e32 v219, v111
	v_fma_f32 v82, v85, s4, -v188
	v_exp_f32_e32 v108, v82
	v_exp_f32_e32 v111, v112
	v_fma_f32 v82, v86, s4, -v188
	s_waitcnt lgkmcnt(3)
	v_mfma_f32_32x32x16_f16 v[66:81], v[202:205], v[122:125], v[66:81]
	v_exp_f32_e32 v202, v82
	v_exp_f32_e32 v203, v113
	v_fma_f32 v82, v87, s4, -v188
	v_exp_f32_e32 v110, v82
	s_waitcnt lgkmcnt(2)
	v_mfma_f32_32x32x16_f16 v[66:81], v[206:209], v[126:129], v[66:81]
	s_waitcnt vmcnt(3)
	ds_write_b128 v185, v[88:91] offset:18432
	s_waitcnt vmcnt(2)
	ds_write_b128 v185, v[92:95] offset:27648
	s_waitcnt vmcnt(1)
	ds_write_b128 v185, v[150:153] offset:36864
	s_waitcnt vmcnt(0)
	ds_write_b128 v185, v[154:157] offset:46080
	v_fma_f32 v150, v176, v166, v97
	v_fma_f32 v151, v176, v96, v167
	v_mfma_f32_32x32x16_f16 v[82:97], v[194:197], v[130:133], 0
	v_fma_f32 v152, v176, v168, v99
	v_fma_f32 v153, v176, v98, v169
	v_fma_f32 v154, v176, v210, v101
	v_fma_f32 v155, v176, v100, v211
	v_fma_f32 v156, v176, v212, v103
	v_fma_f32 v157, v176, v102, v213
	v_fma_f32 v158, v176, v214, v105
	v_fma_f32 v159, v176, v104, v215
	v_fma_f32 v160, v176, v216, v107
	v_fma_f32 v161, v176, v106, v217
	v_fma_f32 v166, v176, v218, v109
	v_fma_f32 v167, v176, v108, v219
	v_fma_f32 v168, v176, v202, v111
	v_fma_f32 v169, v176, v110, v203
	ds_read_b128 v[98:101], v189
	ds_read_b128 v[102:105], v189 offset:1152
	ds_read_b128 v[106:109], v189 offset:2304
	ds_read_b128 v[110:113], v189 offset:3456
	ds_write_b128 v190, v[150:153]
	ds_write_b128 v190, v[154:157] offset:16
	ds_write_b128 v190, v[158:161] offset:64
	ds_write_b128 v190, v[166:169] offset:80
	v_cvt_pk_f16_f32 v157, v156, v157
	v_cvt_pk_f16_f32 v156, v154, v155
	v_cvt_pk_f16_f32 v155, v152, v153
	v_cvt_pk_f16_f32 v154, v150, v151
	ds_read_b128 v[150:153], v191 offset:55296
	ds_read_b128 v[194:197], v191 offset:55328
	v_mfma_f32_32x32x16_f16 v[82:97], v[198:201], v[134:137], v[82:97]
	s_and_b32 s2, s20, 0x7c0
	s_min_u32 s20, s19, 27
	s_lshl_b32 s2, s2, 2
	s_add_i32 s20, s18, s20
	v_lshl_add_u64 v[210:211], v[174:175], 0, s[2:3]
	s_lshl_b32 s2, s20, 13
	s_and_b32 s2, s2, 0x3e000
	s_waitcnt lgkmcnt(1)
	v_mfma_f32_32x32x16_f16 v[50:65], v[154:157], v[150:153], v[50:65]
	ds_read_b128 v[150:153], v191 offset:59904
	ds_read_b128 v[198:201], v191 offset:59936
	s_lshl_b32 s21, s21, 7
	v_cvt_pk_f16_f32 v169, v168, v169
	v_cvt_pk_f16_f32 v168, v166, v167
	v_cvt_pk_f16_f32 v166, v158, v159
	v_cvt_pk_f16_f32 v167, v160, v161
	s_addk_i32 s1, 0x80
	s_waitcnt lgkmcnt(1)
	v_mfma_f32_32x32x16_f16 v[34:49], v[154:157], v[150:153], v[34:49]
	ds_read_b128 v[150:153], v191 offset:64512
	ds_read_b128 v[202:205], v191 offset:64544
	s_waitcnt lgkmcnt(1)
	v_mfma_f32_32x32x16_f16 v[18:33], v[154:157], v[150:153], v[18:33]
	ds_read_b128 v[150:153], v192 offset:13824
	ds_read_b128 v[206:209], v192 offset:13856
	v_mfma_f32_32x32x16_f16 v[82:97], v[146:149], v[138:141], v[82:97]
	v_lshl_add_u64 v[146:147], v[170:171], 0, s[2:3]
	s_and_b32 s2, s21, 0xf80
	v_lshl_add_u64 v[158:159], v[172:173], 0, s[2:3]
	s_add_i32 s2, s19, 2
	s_cmp_lt_u32 s19, 30
	s_mov_b32 s19, s2
	s_waitcnt lgkmcnt(1)
	v_mfma_f32_32x32x16_f16 v[2:17], v[154:157], v[150:153], v[2:17]
	v_add_co_u32_e32 v150, vcc, s15, v146
	s_nop 1
	v_addc_co_u32_e32 v151, vcc, 0, v147, vcc
	global_load_dwordx4 v[146:149], v[146:147], off
	s_nop 0
	global_load_dwordx4 v[150:153], v[150:151], off
	s_nop 0
	global_load_dwordx4 v[154:157], v[158:159], off
	v_add_co_u32_e32 v158, vcc, s10, v158
	v_mfma_f32_32x32x16_f16 v[50:65], v[166:169], v[194:197], v[50:65]
	s_nop 0
	v_addc_co_u32_e32 v159, vcc, 0, v159, vcc
	global_load_dwordx4 v[158:161], v[158:159], off
	v_add_co_u32_e32 v194, vcc, s5, v210
	s_nop 1
	v_addc_co_u32_e32 v195, vcc, 0, v211, vcc
	v_mfma_f32_32x32x16_f16 v[34:49], v[166:169], v[198:201], v[34:49]
	v_add_co_u32_e32 v196, vcc, s13, v210
	s_nop 1
	v_addc_co_u32_e32 v197, vcc, 0, v211, vcc
	v_mfma_f32_32x32x16_f16 v[18:33], v[166:169], v[202:205], v[18:33]
	s_waitcnt lgkmcnt(0)
	v_mfma_f32_32x32x16_f16 v[2:17], v[166:169], v[206:209], v[2:17]
	v_add_co_u32_e32 v166, vcc, s14, v210
	s_nop 1
	v_addc_co_u32_e32 v167, vcc, 0, v211, vcc
	global_store_dwordx4 v[210:211], v[98:101], off nt
	global_store_dwordx4 v[194:195], v[102:105], off nt
	global_store_dwordx4 v[196:197], v[106:109], off nt
	global_store_dwordx4 v[166:167], v[110:113], off nt
	v_mfma_f32_32x32x16_f16 v[82:97], v[162:165], v[142:145], v[82:97]
	s_barrier
	s_cbranch_scc1 .LBB4_7
	s_branch .Ll2_post
	.p2alignl 6, 3212836864
	s_nop 0
	s_nop 0
	s_nop 0
	s_nop 0
.Ll2f_top:
	v_exp_f32_e32 v215, v66
	s_nop 7
	v_exp_f32_e32 v216, v82
	v_exp_f32_e32 v217, v67
	v_exp_f32_e32 v214, v83
	v_exp_f32_e32 v219, v68
	v_exp_f32_e32 v220, v84
	ds_read_b128 v[98:101], v186 offset:18432
	ds_read_b128 v[162:165], v186 offset:18464
	ds_read_b128 v[194:197], v186 offset:27648
	ds_read_b128 v[198:201], v186 offset:27680
	ds_read_b128 v[202:205], v186 offset:18496
	ds_read_b128 v[206:209], v186 offset:18528
	ds_read_b128 v[210:213], v186 offset:27712
	ds_read_b128 v[166:169], v186 offset:27744
	v_exp_f32_e32 v221, v69
	v_exp_f32_e32 v218, v85
	s_waitcnt lgkmcnt(7)
	v_mfma_f32_32x32x16_f16 v[98:113], v[98:101], v[114:117], v[240:255]
	v_exp_f32_e32 v223, v70
	v_exp_f32_e32 v70, v86
	v_exp_f32_e32 v71, v71
	v_exp_f32_e32 v222, v87
	v_exp_f32_e32 v225, v72
	v_exp_f32_e32 v226, v88
	v_exp_f32_e32 v227, v73
	v_exp_f32_e32 v224, v89
	s_waitcnt lgkmcnt(6)
	v_mfma_f32_32x32x16_f16 v[98:113], v[162:165], v[118:121], v[98:113]
	v_exp_f32_e32 v229, v74
	v_exp_f32_e32 v230, v90
	v_exp_f32_e32 v231, v75
	v_exp_f32_e32 v228, v91
	v_exp_f32_e32 v233, v76
	v_exp_f32_e32 v234, v92
	v_exp_f32_e32 v235, v77
	v_exp_f32_e32 v232, v93
	s_waitcnt lgkmcnt(3)
	v_mfma_f32_32x32x16_f16 v[98:113], v[202:205], v[122:125], v[98:113]
	v_exp_f32_e32 v237, v78
	v_exp_f32_e32 v162, v94
	v_exp_f32_e32 v163, v79
	v_exp_f32_e32 v236, v95
	v_exp_f32_e32 v165, v80
	v_exp_f32_e32 v202, v96
	v_exp_f32_e32 v203, v81
	v_exp_f32_e32 v193, v97
	s_waitcnt lgkmcnt(2)
	v_mfma_f32_32x32x16_f16 v[98:113], v[206:209], v[126:129], v[98:113]
	s_waitcnt vmcnt(3)
	ds_write_b128 v185, v[146:149]
	s_waitcnt vmcnt(2)
	ds_write_b128 v185, v[150:153] offset:9216
	s_waitcnt vmcnt(1)
	ds_write_b128 v185, v[154:157] offset:55296
	s_waitcnt vmcnt(0)
	ds_write_b128 v185, v[158:161] offset:64512
	v_fma_f32 v150, v176, v216, v215
	v_fma_f32 v151, v176, v214, v217
	ds_read_b128 v[66:69], v189
	ds_read_b128 v[88:91], v189 offset:1152
	v_fma_f32 v152, v176, v220, v219
	v_fma_f32 v153, v176, v218, v221
	ds_read_b128 v[92:95], v189 offset:2304
	ds_read_b128 v[146:149], v189 offset:3456
	v_fma_f32 v154, v176, v70, v223
	v_fma_f32 v155, v176, v222, v71
	ds_write_b128 v190, v[150:153]
	v_fma_f32 v156, v176, v226, v225
	v_fma_f32 v157, v176, v224, v227
	ds_write_b128 v190, v[154:157] offset:16
	v_fma_f32 v158, v176, v230, v229
	v_fma_f32 v159, v176, v228, v231
	v_cvt_pk_f16_f32 v157, v156, v157
	v_fma_f32 v160, v176, v234, v233
	v_fma_f32 v161, v176, v232, v235
	ds_write_b128 v190, v[158:161] offset:64
	v_fma_f32 v162, v176, v162, v237
	v_fma_f32 v163, v176, v236, v163
	v_cvt_pk_f16_f32 v156, v154, v155
	v_fma_f32 v164, v176, v202, v165
	v_fma_f32 v165, v176, v193, v203
	ds_write_b128 v190, v[162:165] offset:80
	v_cvt_pk_f16_f32 v155, v152, v153
	v_cvt_pk_f16_f32 v154, v150, v151
	ds_read_b128 v[150:153], v191 offset:36864
	s_cmp_eq_u32 s19, 0
	s_cselect_b64 vcc, -1, 0
	s_add_i32 s20, s16, s1
	v_mfma_f32_32x32x16_f16 v[72:87], v[194:197], v[130:133], 0
	ds_read_b128 v[194:197], v191 offset:36896
	s_add_i32 s2, s20, 0x7c0
	s_and_b32 s2, s2, 0x7c0
	s_lshl_b32 s2, s2, 2
	v_lshl_add_u64 v[70:71], v[174:175], 0, s[2:3]
	v_cndmask_b32_e32 v71, v71, v179, vcc
	v_cndmask_b32_e32 v70, v70, v178, vcc
	s_waitcnt lgkmcnt(1)
	v_mfma_f32_32x32x16_f16 v[50:65], v[154:157], v[150:153], v[50:65]
	ds_read_b128 v[150:153], v191 offset:41472
	global_store_dwordx4 v[70:71], v[66:69], off nt
	ds_read_b128 v[66:69], v191 offset:41504
	v_cvt_pk_f16_f32 v165, v164, v165
	v_cvt_pk_f16_f32 v164, v162, v163
	v_cvt_pk_f16_f32 v163, v160, v161
	v_cvt_pk_f16_f32 v162, v158, v159
	s_waitcnt lgkmcnt(1)
	v_mfma_f32_32x32x16_f16 v[34:49], v[154:157], v[150:153], v[34:49]
	v_add_co_u32_e32 v96, vcc, s5, v70
	s_min_u32 s2, s19, 28
	s_nop 0
	v_addc_co_u32_e32 v97, vcc, 0, v71, vcc
	global_store_dwordx4 v[96:97], v[88:91], off nt
	s_add_i32 s21, s17, s2
	s_waitcnt lgkmcnt(0)
	v_mfma_f32_32x32x16_f16 v[34:49], v[162:165], v[66:69], v[34:49]
	ds_read_b128 v[66:69], v191 offset:46080
	v_add_co_u32_e32 v88, vcc, s13, v70
	s_lshl_b32 s2, s21, 13
	s_nop 0
	v_addc_co_u32_e32 v89, vcc, 0, v71, vcc
	global_store_dwordx4 v[88:89], v[92:95], off nt
	ds_read_b128 v[88:91], v191 offset:46112
	s_waitcnt lgkmcnt(1)
	v_mfma_f32_32x32x16_f16 v[18:33], v[154:157], v[66:69], v[18:33]
	v_add_co_u32_e32 v70, vcc, s14, v70
	s_and_b32 s2, s2, 0x3e000
	s_nop 0
	v_addc_co_u32_e32 v71, vcc, 0, v71, vcc
	v_lshl_add_u64 v[66:67], v[170:171], 0, s[2:3]
	v_add_co_u32_e32 v68, vcc, s15, v66
	global_store_dwordx4 v[70:71], v[146:149], off nt
	s_nop 0
	v_addc_co_u32_e32 v69, vcc, 0, v67, vcc
	s_waitcnt lgkmcnt(0)
	v_mfma_f32_32x32x16_f16 v[18:33], v[162:165], v[88:91], v[18:33]
	global_load_dwordx4 v[88:91], v[66:67], off
	global_load_dwordx4 v[92:95], v[68:69], off
	ds_read_b128 v[66:69], v191 offset:50688
	ds_read_b128 v[146:149], v191 offset:50720
	s_min_u32 s2, s19, 29
	s_add_i32 s2, s0, s2
	s_lshl_b32 s2, s2, 7
	s_and_b32 s2, s2, 0xf80
	s_waitcnt lgkmcnt(1)
	v_mfma_f32_32x32x16_f16 v[2:17], v[154:157], v[66:69], v[2:17]
	v_lshl_add_u64 v[66:67], v[172:173], 0, s[2:3]
	v_add_co_u32_e32 v68, vcc, s10, v66
	s_nop 0
	v_addc_co_u32_e32 v69, vcc, 0, v67, vcc
	global_load_dwordx4 v[150:153], v[66:67], off
	global_load_dwordx4 v[154:157], v[68:69], off
	v_mfma_f32_32x32x16_f16 v[72:87], v[198:201], v[134:137], v[72:87]
	v_exp_f32_e32 v97, v98
	s_waitcnt lgkmcnt(0)
	s_barrier
	v_mfma_f32_32x32x16_f16 v[72:87], v[210:213], v[138:141], v[72:87]
	v_mfma_f32_32x32x16_f16 v[72:87], v[166:169], v[142:145], v[72:87]
	v_mfma_f32_32x32x16_f16 v[50:65], v[162:165], v[194:197], v[50:65]
	s_nop 10
	v_exp_f32_e32 v166, v72
	v_exp_f32_e32 v167, v99
	v_exp_f32_e32 v96, v73
	v_exp_f32_e32 v99, v100
	v_exp_f32_e32 v168, v74
	v_exp_f32_e32 v169, v101
	v_exp_f32_e32 v98, v75
	v_exp_f32_e32 v101, v102
	v_exp_f32_e32 v210, v76
	v_exp_f32_e32 v211, v103
	v_exp_f32_e32 v100, v77
	v_exp_f32_e32 v103, v104
	v_exp_f32_e32 v212, v78
	v_exp_f32_e32 v213, v105
	v_exp_f32_e32 v102, v79
	v_exp_f32_e32 v105, v106
	v_exp_f32_e32 v214, v80
	v_exp_f32_e32 v215, v107
	v_mfma_f32_32x32x16_f16 v[2:17], v[162:165], v[146:149], v[2:17]
	ds_read_b128 v[66:69], v186
	ds_read_b128 v[158:161], v186 offset:32
	ds_read_b128 v[194:197], v186 offset:9216
	ds_read_b128 v[198:201], v186 offset:9248
	ds_read_b128 v[202:205], v186 offset:64
	ds_read_b128 v[206:209], v186 offset:96
	ds_read_b128 v[146:149], v186 offset:9280
	ds_read_b128 v[162:165], v186 offset:9312
	v_exp_f32_e32 v104, v81
	v_exp_f32_e32 v107, v108
	v_exp_f32_e32 v216, v82
	s_waitcnt lgkmcnt(7)
	v_mfma_f32_32x32x16_f16 v[66:81], v[66:69], v[114:117], v[240:255]
	v_exp_f32_e32 v217, v109
	v_exp_f32_e32 v106, v83
	v_exp_f32_e32 v109, v110
	v_exp_f32_e32 v218, v84
	s_waitcnt lgkmcnt(6)
	v_mfma_f32_32x32x16_f16 v[66:81], v[158:161], v[118:121], v[66:81]
	v_exp_f32_e32 v219, v111
	v_exp_f32_e32 v108, v85
	v_exp_f32_e32 v111, v112
	s_waitcnt lgkmcnt(3)
	v_mfma_f32_32x32x16_f16 v[66:81], v[202:205], v[122:125], v[66:81]
	v_exp_f32_e32 v202, v86
	v_exp_f32_e32 v203, v113
	v_exp_f32_e32 v110, v87
	s_waitcnt lgkmcnt(2)
	v_mfma_f32_32x32x16_f16 v[66:81], v[206:209], v[126:129], v[66:81]
	s_waitcnt vmcnt(3)
	ds_write_b128 v185, v[88:91] offset:18432
	s_waitcnt vmcnt(2)
	ds_write_b128 v185, v[92:95] offset:27648
	s_waitcnt vmcnt(1)
	ds_write_b128 v185, v[150:153] offset:36864
	s_waitcnt vmcnt(0)
	ds_write_b128 v185, v[154:157] offset:46080
	v_fma_f32 v150, v176, v166, v97
	v_fma_f32 v151, v176, v96, v167
	v_mfma_f32_32x32x16_f16 v[82:97], v[194:197], v[130:133], 0
	v_fma_f32 v152, v176, v168, v99
	v_fma_f32 v153, v176, v98, v169
	v_fma_f32 v154, v176, v210, v101
	v_fma_f32 v155, v176, v100, v211
	v_fma_f32 v156, v176, v212, v103
	v_fma_f32 v157, v176, v102, v213
	v_fma_f32 v158, v176, v214, v105
	v_fma_f32 v159, v176, v104, v215
	v_fma_f32 v160, v176, v216, v107
	v_fma_f32 v161, v176, v106, v217
	v_fma_f32 v166, v176, v218, v109
	v_fma_f32 v167, v176, v108, v219
	v_fma_f32 v168, v176, v202, v111
	v_fma_f32 v169, v176, v110, v203
	ds_read_b128 v[98:101], v189
	ds_read_b128 v[102:105], v189 offset:1152
	ds_read_b128 v[106:109], v189 offset:2304
	ds_read_b128 v[110:113], v189 offset:3456
	ds_write_b128 v190, v[150:153]
	ds_write_b128 v190, v[154:157] offset:16
	ds_write_b128 v190, v[158:161] offset:64
	ds_write_b128 v190, v[166:169] offset:80
	v_cvt_pk_f16_f32 v157, v156, v157
	v_cvt_pk_f16_f32 v156, v154, v155
	v_cvt_pk_f16_f32 v155, v152, v153
	v_cvt_pk_f16_f32 v154, v150, v151
	ds_read_b128 v[150:153], v191 offset:55296
	ds_read_b128 v[194:197], v191 offset:55328
	v_mfma_f32_32x32x16_f16 v[82:97], v[198:201], v[134:137], v[82:97]
	s_and_b32 s2, s20, 0x7c0
	s_min_u32 s20, s19, 27
	s_lshl_b32 s2, s2, 2
	s_add_i32 s20, s18, s20
	v_lshl_add_u64 v[210:211], v[174:175], 0, s[2:3]
	s_lshl_b32 s2, s20, 13
	s_and_b32 s2, s2, 0x3e000
	s_waitcnt lgkmcnt(1)
	v_mfma_f32_32x32x16_f16 v[50:65], v[154:157], v[150:153], v[50:65]
	ds_read_b128 v[150:153], v191 offset:59904
	ds_read_b128 v[198:201], v191 offset:59936
	s_lshl_b32 s21, s21, 7
	v_cvt_pk_f16_f32 v169, v168, v169
	v_cvt_pk_f16_f32 v168, v166, v167
	v_cvt_pk_f16_f32 v166, v158, v159
	v_cvt_pk_f16_f32 v167, v160, v161
	s_addk_i32 s1, 0x80
	s_waitcnt lgkmcnt(1)
	v_mfma_f32_32x32x16_f16 v[34:49], v[154:157], v[150:153], v[34:49]
	ds_read_b128 v[150:153], v191 offset:64512
	ds_read_b128 v[202:205], v191 offset:64544
	s_waitcnt lgkmcnt(1)
	v_mfma_f32_32x32x16_f16 v[18:33], v[154:157], v[150:153], v[18:33]
	ds_read_b128 v[150:153], v192 offset:13824
	ds_read_b128 v[206:209], v192 offset:13856
	v_mfma_f32_32x32x16_f16 v[82:97], v[146:149], v[138:141], v[82:97]
	v_lshl_add_u64 v[146:147], v[170:171], 0, s[2:3]
	s_and_b32 s2, s21, 0xf80
	v_lshl_add_u64 v[158:159], v[172:173], 0, s[2:3]
	s_add_i32 s2, s19, 2
	s_cmp_lt_u32 s19, 30
	s_mov_b32 s19, s2
	s_waitcnt lgkmcnt(1)
	v_mfma_f32_32x32x16_f16 v[2:17], v[154:157], v[150:153], v[2:17]
	v_add_co_u32_e32 v150, vcc, s15, v146
	s_nop 1
	v_addc_co_u32_e32 v151, vcc, 0, v147, vcc
	global_load_dwordx4 v[146:149], v[146:147], off
	s_nop 0
	global_load_dwordx4 v[150:153], v[150:151], off
	s_nop 0
	global_load_dwordx4 v[154:157], v[158:159], off
	v_add_co_u32_e32 v158, vcc, s10, v158
	v_mfma_f32_32x32x16_f16 v[50:65], v[166:169], v[194:197], v[50:65]
	s_nop 0
	v_addc_co_u32_e32 v159, vcc, 0, v159, vcc
	global_load_dwordx4 v[158:161], v[158:159], off
	v_add_co_u32_e32 v194, vcc, s5, v210
	s_nop 1
	v_addc_co_u32_e32 v195, vcc, 0, v211, vcc
	v_mfma_f32_32x32x16_f16 v[34:49], v[166:169], v[198:201], v[34:49]
	v_add_co_u32_e32 v196, vcc, s13, v210
	s_nop 1
	v_addc_co_u32_e32 v197, vcc, 0, v211, vcc
	v_mfma_f32_32x32x16_f16 v[18:33], v[166:169], v[202:205], v[18:33]
	s_waitcnt lgkmcnt(0)
	v_mfma_f32_32x32x16_f16 v[2:17], v[166:169], v[206:209], v[2:17]
	v_add_co_u32_e32 v166, vcc, s14, v210
	s_nop 1
	v_addc_co_u32_e32 v167, vcc, 0, v211, vcc
	global_store_dwordx4 v[210:211], v[98:101], off nt
	global_store_dwordx4 v[194:195], v[102:105], off nt
	global_store_dwordx4 v[196:197], v[106:109], off nt
	global_store_dwordx4 v[166:167], v[110:113], off nt
	v_mfma_f32_32x32x16_f16 v[82:97], v[162:165], v[142:145], v[82:97]
	s_barrier
	s_cbranch_scc1 .Ll2f_top
.Ll2_post:
	ds_read_b128 v[66:69], v189
	ds_read_b128 v[70:73], v189 offset:1152
	s_addk_i32 s11, 0x7c0
	s_and_b32 s0, s11, 0x7c0
	s_lshl_b32 s0, s0, 2
	s_mov_b32 s1, 0
	v_lshl_add_u64 v[74:75], v[174:175], 0, s[0:1]
	s_waitcnt lgkmcnt(1)
	global_store_dwordx4 v[74:75], v[66:69], off nt
	s_mov_b32 s0, 0x10800
	v_lshlrev_b32_e32 v1, 2, v1
	v_add_co_u32_e32 v66, vcc, 0x10000, v74
	v_lshrrev_b32_e32 v86, 2, v0
	s_nop 0
	v_addc_co_u32_e32 v67, vcc, 0, v75, vcc
	s_waitcnt lgkmcnt(0)
	global_store_dwordx4 v[66:67], v[70:73], off nt
	ds_read_b128 v[66:69], v189 offset:2304
	ds_read_b128 v[70:73], v189 offset:3456
	v_add_co_u32_e32 v76, vcc, 0x20000, v74
	v_lshlrev_b32_e32 v0, 5, v0
	s_nop 0
	v_addc_co_u32_e32 v77, vcc, 0, v75, vcc
	s_waitcnt lgkmcnt(1)
	global_store_dwordx4 v[76:77], v[66:69], off nt
	v_and_b32_e32 v87, 0x60, v0
	v_lshlrev_b32_e32 v88, 2, v87
	v_add_co_u32_e32 v66, vcc, 0x30000, v74
	s_nop 1
	v_addc_co_u32_e32 v67, vcc, 0, v75, vcc
	s_waitcnt lgkmcnt(0)
	global_store_dwordx4 v[66:67], v[70:73], off nt
	v_lshl_or_b32 v67, v182, 2, v183
	v_mad_u32_u24 v66, v184, s0, 0
	v_mul_u32_u24_e32 v67, 0x210, v67
	v_add3_u32 v1, v66, v1, v67
	s_barrier
	ds_write2_b32 v1, v50, v34 offset1:32
	ds_write2_b32 v1, v51, v35 offset0:132 offset1:164
	v_add_u32_e32 v34, 0x400, v1
	ds_write2_b32 v34, v52, v36 offset0:8 offset1:40
	ds_write2_b32 v34, v53, v37 offset0:140 offset1:172
	v_add_u32_e32 v35, 0x1000, v1
	v_add_u32_e32 v36, 0x1400, v1
	ds_write2_b32 v35, v54, v38 offset0:32 offset1:64
	ds_write2_b32 v35, v55, v39 offset0:164 offset1:196
	ds_write2_b32 v36, v56, v40 offset0:40 offset1:72
	ds_write2_b32 v36, v57, v41 offset0:172 offset1:204
	v_add_u32_e32 v37, 0x2000, v1
	v_add_u32_e32 v38, 0x2400, v1
	v_add_u32_e32 v40, 0x3200, v1
	ds_write2_b32 v37, v58, v42 offset0:64 offset1:96
	ds_write2_b32 v37, v59, v43 offset0:196 offset1:228
	ds_write2_b32 v38, v60, v44 offset0:72 offset1:104
	ds_write2_b32 v38, v61, v45 offset0:204 offset1:236
	v_add_u32_e32 v39, 0x3000, v1
	ds_write2_b32 v40, v63, v47 offset0:100 offset1:132
	v_add_u32_e32 v40, 0x3400, v1
	v_add_u32_e32 v41, 0x3600, v1
	ds_write2_b32 v39, v62, v46 offset0:96 offset1:128
	ds_write2_b32 v40, v64, v48 offset0:104 offset1:136
	ds_write2_b32 v41, v65, v49 offset0:108 offset1:140
	ds_write2_b32 v1, v18, v2 offset0:64 offset1:96
	ds_write2_b32 v1, v19, v3 offset0:196 offset1:228
	ds_write2_b32 v34, v20, v4 offset0:72 offset1:104
	ds_write2_b32 v34, v21, v5 offset0:204 offset1:236
	ds_write2_b32 v35, v22, v6 offset0:96 offset1:128
	v_add_u32_e32 v2, 0x1200, v1
	ds_write2_b32 v2, v23, v7 offset0:100 offset1:132
	ds_write2_b32 v36, v24, v8 offset0:104 offset1:136
	v_add_u32_e32 v2, 0x1600, v1
	ds_write2_b32 v2, v25, v9 offset0:108 offset1:140
	ds_write2_b32 v37, v26, v10 offset0:128 offset1:160
	ds_write2_b32 v38, v27, v11 offset0:4 offset1:36
	ds_write2_b32 v38, v28, v12 offset0:136 offset1:168
	v_add_u32_e32 v2, 0x2800, v1
	v_add_u32_e32 v1, 0x3800, v1
	ds_write2_b32 v2, v29, v13 offset0:12 offset1:44
	ds_write2_b32 v39, v30, v14 offset0:160 offset1:192
	ds_write2_b32 v40, v31, v15 offset0:36 offset1:68
	ds_write2_b32 v40, v32, v16 offset0:168 offset1:200
	ds_write2_b32 v1, v33, v17 offset0:44 offset1:76
	v_mul_u32_u24_e32 v1, 0x210, v86
	v_add3_u32 v89, 0, v1, v88
	v_add_u32_e32 v0, 0x10800, v89
	s_waitcnt lgkmcnt(0)
	s_barrier
	ds_read_b128 v[10:13], v0
	ds_read_b128 v[14:17], v0 offset:16
	ds_read_b128 v[4:7], v89 offset:16
	ds_read_b128 v[18:21], v89
	v_add_u32_e32 v26, 0x10820, v89
	ds_read_b128 v[22:25], v89 offset:32
	ds_read_b128 v[0:3], v89 offset:48
	v_add_u32_e32 v34, 0x10810, v89
	s_waitcnt lgkmcnt(3)
	v_pk_add_f32 v[16:17], v[6:7], v[16:17]
	v_pk_add_f32 v[14:15], v[4:5], v[14:15]
	s_waitcnt lgkmcnt(2)
	v_pk_add_f32 v[10:11], v[18:19], v[10:11]
	v_pk_add_f32 v[8:9], v[20:21], v[12:13]
	v_pk_mul_f32 v[20:21], v[16:17], v[16:17]
	v_pk_mul_f32 v[16:17], v[10:11], v[10:11]
	v_pk_mul_f32 v[14:15], v[14:15], v[14:15]
	v_pk_mul_f32 v[12:13], v[8:9], v[8:9]
	v_mov_b32_e32 v18, v16
	v_mov_b32_e32 v19, v14
	v_mov_b32_e32 v14, v17
	v_pk_add_f32 v[14:15], v[18:19], v[14:15]
	v_mov_b32_e32 v16, v12
	v_mov_b32_e32 v17, v20
	v_pk_add_f32 v[18:19], v[14:15], v[16:17]
	v_mov_b32_e32 v20, v13
	ds_read_b128 v[14:17], v26 offset:16
	v_pk_add_f32 v[12:13], v[18:19], v[20:21]
	ds_read_b128 v[18:21], v26
	v_add_u32_e32 v38, 0x10840, v89
	ds_read_b128 v[26:29], v38
	s_waitcnt lgkmcnt(2)
	v_pk_add_f32 v[32:33], v[0:1], v[14:15]
	v_pk_add_f32 v[30:31], v[2:3], v[16:17]
	s_waitcnt lgkmcnt(1)
	v_pk_add_f32 v[80:81], v[22:23], v[18:19]
	v_pk_add_f32 v[78:79], v[24:25], v[20:21]
	v_pk_mul_f32 v[18:19], v[80:81], v[80:81]
	v_pk_mul_f32 v[22:23], v[32:33], v[32:33]
	v_pk_mul_f32 v[20:21], v[78:79], v[78:79]
	v_pk_mul_f32 v[30:31], v[30:31], v[30:31]
	v_mov_b32_e32 v24, v18
	v_mov_b32_e32 v25, v22
	v_mov_b32_e32 v22, v19
	v_pk_add_f32 v[18:19], v[24:25], v[22:23]
	v_mov_b32_e32 v22, v20
	v_mov_b32_e32 v23, v30
	ds_read_b128 v[14:17], v34
	v_pk_add_f32 v[32:33], v[18:19], v[22:23]
	v_mov_b32_e32 v30, v21
	ds_read_b128 v[18:21], v89 offset:80
	ds_read_b128 v[22:25], v38 offset:16
	v_pk_add_f32 v[82:83], v[32:33], v[30:31]
	ds_read_b128 v[30:33], v89 offset:64
	ds_read_b128 v[34:37], v89 offset:80
	ds_read_b128 v[38:41], v38
	ds_read_b128 v[42:45], v89 offset:64
	v_add_u32_e32 v74, 0x10860, v89
	s_waitcnt lgkmcnt(4)
	v_pk_add_f32 v[20:21], v[20:21], v[24:25]
	v_pk_add_f32 v[18:19], v[18:19], v[22:23]
	s_waitcnt lgkmcnt(3)
	v_pk_add_f32 v[22:23], v[30:31], v[26:27]
	v_pk_add_f32 v[24:25], v[32:33], v[28:29]
	v_pk_mul_f32 v[28:29], v[20:21], v[20:21]
	v_pk_mul_f32 v[20:21], v[22:23], v[22:23]
	v_pk_mul_f32 v[30:31], v[18:19], v[18:19]
	v_pk_mul_f32 v[26:27], v[24:25], v[24:25]
	v_mov_b32_e32 v32, v20
	v_mov_b32_e32 v33, v30
	v_mov_b32_e32 v30, v21
	global_load_dwordx4 v[18:21], v88, s[8:9] offset:16
	global_load_dwordx4 v[22:25], v88, s[8:9]
	v_pk_add_f32 v[30:31], v[32:33], v[30:31]
	v_mov_b32_e32 v32, v26
	v_mov_b32_e32 v33, v28
	v_pk_add_f32 v[30:31], v[30:31], v[32:33]
	v_mov_b32_e32 v28, v27
	v_pk_add_f32 v[84:85], v[30:31], v[28:29]
	ds_read_b128 v[26:29], v89 offset:96
	ds_read_b128 v[30:33], v89 offset:112
	ds_read_b128 v[46:49], v74
	ds_read_b128 v[50:53], v74 offset:16
	global_load_dwordx4 v[54:57], v88, s[8:9] offset:48
	global_load_dwordx4 v[58:61], v88, s[8:9] offset:32
	v_add_u32_e32 v62, 0x10830, v89
	ds_read_b128 v[62:65], v62
	ds_read_b128 v[66:69], v89 offset:112
	s_waitcnt lgkmcnt(3)
	v_pk_add_f32 v[28:29], v[28:29], v[48:49]
	s_waitcnt lgkmcnt(2)
	v_pk_add_f32 v[30:31], v[30:31], v[50:51]
	v_pk_add_f32 v[26:27], v[26:27], v[46:47]
	v_pk_mul_f32 v[46:47], v[28:29], v[28:29]
	v_pk_mul_f32 v[26:27], v[26:27], v[26:27]
	v_pk_mul_f32 v[28:29], v[30:31], v[30:31]
	v_pk_add_f32 v[32:33], v[32:33], v[52:53]
	v_mov_b32_e32 v30, v26
	v_mov_b32_e32 v31, v28
	v_mov_b32_e32 v28, v27
	ds_read_b128 v[70:73], v89 offset:96
	ds_read_b128 v[74:77], v74
	v_pk_mul_f32 v[48:49], v[32:33], v[32:33]
	v_pk_add_f32 v[50:51], v[30:31], v[28:29]
	global_load_dwordx4 v[26:29], v88, s[8:9] offset:80
	global_load_dwordx4 v[30:33], v88, s[8:9] offset:64
	v_add_f32_e32 v12, v12, v13
	v_add_f32_e32 v12, v12, v82
	v_mov_b32_e32 v52, v46
	v_mov_b32_e32 v53, v48
	v_add_f32_e32 v12, v12, v83
	v_pk_add_f32 v[50:51], v[50:51], v[52:53]
	v_mov_b32_e32 v48, v47
	v_add_f32_e32 v12, v12, v84
	v_pk_add_f32 v[46:47], v[50:51], v[48:49]
	v_add_f32_e32 v12, v12, v85
	v_add_f32_e32 v12, v12, v46
	v_add_f32_e32 v12, v12, v47
	global_load_dwordx4 v[46:49], v88, s[8:9] offset:96
	global_load_dwordx4 v[50:53], v88, s[8:9] offset:112
	ds_bpermute_b32 v13, v181, v12
	s_mov_b32 s0, 0x800000
	v_pk_add_f32 v[4:5], v[4:5], v[14:15]
	s_waitcnt lgkmcnt(4)
	v_pk_add_f32 v[0:1], v[0:1], v[62:63]
	s_waitcnt lgkmcnt(0)
	v_add_f32_e32 v12, v12, v13
	ds_bpermute_b32 v13, v180, v12
	s_waitcnt lgkmcnt(0)
	v_add_f32_e32 v12, v12, v13
	v_mov_b32_e32 v13, 0x3727c5ac
	v_fmac_f32_e32 v13, 0x3c000000, v12
	v_mul_f32_e32 v12, 0x4b800000, v13
	v_cmp_gt_f32_e32 vcc, s0, v13
	s_lshl_b32 s0, s12, 1
	s_nop 0
	v_cndmask_b32_e32 v12, v13, v12, vcc
	v_rsq_f32_e32 v12, v12
	s_nop 0
	v_mul_f32_e32 v13, 0x45800000, v12
	v_cndmask_b32_e32 v12, v12, v13, vcc
	v_mul_f32_e32 v82, 0x3f4ccccd, v12
	v_add_u32_e32 v12, s16, v86
	v_mov_b32_e32 v13, 0
	v_lshlrev_b64 v[84:85], 12, v[12:13]
	v_lshl_add_u64 v[84:85], s[6:7], 0, v[84:85]
	v_pk_mul_f32 v[4:5], v[82:83], v[4:5] op_sel_hi:[0,1]
	v_lshl_add_u64 v[84:85], v[84:85], 0, s[0:1]
	v_lshlrev_b32_e32 v12, 1, v87
	v_lshl_add_u64 v[84:85], v[84:85], 0, v[12:13]
	v_pk_mul_f32 v[0:1], v[82:83], v[0:1] op_sel_hi:[0,1]
	v_pk_mul_f32 v[10:11], v[82:83], v[10:11] op_sel_hi:[0,1]
	v_pk_mul_f32 v[8:9], v[82:83], v[8:9] op_sel_hi:[0,1]
	s_waitcnt vmcnt(7)
	v_pk_mul_f32 v[4:5], v[4:5], v[18:19]
	s_nop 0
	v_cvt_pk_f16_f32 v12, v4, v5
	v_pk_add_f32 v[4:5], v[6:7], v[16:17]
	v_pk_mul_f32 v[6:7], v[82:83], v[78:79] op_sel_hi:[0,1]
	v_pk_mul_f32 v[4:5], v[82:83], v[4:5] op_sel_hi:[0,1]
	v_pk_mul_f32 v[4:5], v[4:5], v[20:21]
	s_waitcnt vmcnt(6)
	v_pk_mul_f32 v[10:11], v[10:11], v[22:23]
	v_cvt_pk_f16_f32 v13, v4, v5
	v_pk_mul_f32 v[4:5], v[82:83], v[80:81] op_sel_hi:[0,1]
	s_waitcnt vmcnt(4)
	v_pk_mul_f32 v[4:5], v[4:5], v[58:59]
	v_pk_mul_f32 v[6:7], v[6:7], v[60:61]
	v_pk_mul_f32 v[0:1], v[0:1], v[54:55]
	v_cvt_pk_f16_f32 v4, v4, v5
	v_cvt_pk_f16_f32 v5, v6, v7
	v_cvt_pk_f16_f32 v6, v0, v1
	v_pk_add_f32 v[0:1], v[2:3], v[64:65]
	v_pk_add_f32 v[2:3], v[44:45], v[40:41]
	v_pk_mul_f32 v[0:1], v[82:83], v[0:1] op_sel_hi:[0,1]
	v_pk_mul_f32 v[0:1], v[0:1], v[56:57]
	v_pk_mul_f32 v[8:9], v[8:9], v[24:25]
	v_cvt_pk_f16_f32 v7, v0, v1
	global_store_dwordx4 v[84:85], v[4:7], off offset:16
	v_pk_add_f32 v[0:1], v[42:43], v[38:39]
	v_cvt_pk_f16_f32 v10, v10, v11
	v_add_u32_e32 v4, 0x10850, v89
	v_pk_mul_f32 v[6:7], v[82:83], v[2:3] op_sel_hi:[0,1]
	ds_read_b128 v[2:5], v4
	v_pk_mul_f32 v[0:1], v[82:83], v[0:1] op_sel_hi:[0,1]
	s_waitcnt vmcnt(3)
	v_pk_mul_f32 v[0:1], v[0:1], v[30:31]
	v_pk_mul_f32 v[6:7], v[6:7], v[32:33]
	v_cvt_pk_f16_f32 v0, v0, v1
	v_cvt_pk_f16_f32 v1, v6, v7
	v_add_u32_e32 v6, 0x10870, v89
	v_cvt_pk_f16_f32 v11, v8, v9
	ds_read_b128 v[6:9], v6
	s_waitcnt lgkmcnt(1)
	v_pk_add_f32 v[2:3], v[34:35], v[2:3]
	v_pk_add_f32 v[4:5], v[36:37], v[4:5]
	v_pk_mul_f32 v[2:3], v[82:83], v[2:3] op_sel_hi:[0,1]
	v_pk_mul_f32 v[4:5], v[82:83], v[4:5] op_sel_hi:[0,1]
	v_pk_mul_f32 v[2:3], v[2:3], v[26:27]
	v_pk_mul_f32 v[4:5], v[4:5], v[28:29]
	v_cvt_pk_f16_f32 v2, v2, v3
	v_cvt_pk_f16_f32 v3, v4, v5
	global_store_dwordx4 v[84:85], v[0:3], off offset:32
	s_waitcnt lgkmcnt(0)
	v_pk_add_f32 v[4:5], v[68:69], v[8:9]
	global_store_dwordx4 v[84:85], v[10:13], off
	v_pk_add_f32 v[0:1], v[70:71], v[74:75]
	v_pk_add_f32 v[2:3], v[72:73], v[76:77]
	v_pk_mul_f32 v[0:1], v[82:83], v[0:1] op_sel_hi:[0,1]
	v_pk_mul_f32 v[2:3], v[82:83], v[2:3] op_sel_hi:[0,1]
	s_waitcnt vmcnt(4)
	v_pk_mul_f32 v[0:1], v[0:1], v[46:47]
	v_pk_mul_f32 v[2:3], v[2:3], v[48:49]
	v_cvt_pk_f16_f32 v0, v0, v1
	v_cvt_pk_f16_f32 v1, v2, v3
	v_pk_add_f32 v[2:3], v[66:67], v[6:7]
	v_pk_mul_f32 v[4:5], v[82:83], v[4:5] op_sel_hi:[0,1]
	v_pk_mul_f32 v[2:3], v[82:83], v[2:3] op_sel_hi:[0,1]
	s_waitcnt vmcnt(3)
	v_pk_mul_f32 v[2:3], v[2:3], v[50:51]
	v_pk_mul_f32 v[4:5], v[4:5], v[52:53]
	v_cvt_pk_f16_f32 v2, v2, v3
	v_cvt_pk_f16_f32 v3, v4, v5
	global_store_dwordx4 v[84:85], v[0:3], off offset:48
	s_endpgm

	.amdhsa_kernel _Z11attn_kernelPKDF16_S0_PKfS2_S2_S2_S2_PfPDF16_S3_
		.amdhsa_group_segment_fixed_size 0
		.amdhsa_private_segment_fixed_size 0
		.amdhsa_kernarg_size 80
		.amdhsa_user_sgpr_count 2
		.amdhsa_user_sgpr_dispatch_ptr 0
		.amdhsa_user_sgpr_queue_ptr 0
		.amdhsa_user_sgpr_kernarg_segment_ptr 1
		.amdhsa_user_sgpr_dispatch_id 0
		.amdhsa_user_sgpr_kernarg_preload_length 0
		.amdhsa_user_sgpr_kernarg_preload_offset 0
		.amdhsa_user_sgpr_private_segment_size 0
		.amdhsa_uses_dynamic_stack 0
		.amdhsa_enable_private_segment 0
		.amdhsa_system_sgpr_workgroup_id_x 1
		.amdhsa_system_sgpr_workgroup_id_y 0
		.amdhsa_system_sgpr_workgroup_id_z 0
		.amdhsa_system_sgpr_workgroup_info 0
		.amdhsa_system_vgpr_workitem_id 0
		.amdhsa_next_free_vgpr 256
		.amdhsa_next_free_sgpr 38
		.amdhsa_accum_offset 256
		.amdhsa_reserve_vcc 1
		.amdhsa_float_round_mode_32 0
		.amdhsa_float_round_mode_16_64 0
		.amdhsa_float_denorm_mode_32 3
		.amdhsa_float_denorm_mode_16_64 3
		.amdhsa_dx10_clamp 1
		.amdhsa_ieee_mode 1
		.amdhsa_fp16_overflow 0
		.amdhsa_tg_split 0
		.amdhsa_exception_fp_ieee_invalid_op 0
		.amdhsa_exception_fp_denorm_src 0
		.amdhsa_exception_fp_ieee_div_zero 0
		.amdhsa_exception_fp_ieee_overflow 0
		.amdhsa_exception_fp_ieee_underflow 0
		.amdhsa_exception_fp_ieee_inexact 0
		.amdhsa_exception_int_div_zero 0
	.end_amdhsa_kernel

amdhsa.kernels:
  - .agpr_count:     0
    .args:
      - .actual_access:  read_only
        .address_space:  global
        .offset:         0
        .size:           8
        .value_kind:     global_buffer
      - .actual_access:  write_only
        .address_space:  global
        .offset:         8
        .size:           8
        .value_kind:     global_buffer
    .group_segment_fixed_size: 0
    .kernarg_segment_align: 8
    .kernarg_segment_size: 16
    .language:       OpenCL C
    .language_version:
      - 2
      - 0
    .max_flat_workgroup_size: 256
    .name:           _Z13conv_x_kernelPKfPDF16_
    .private_segment_fixed_size: 0
    .sgpr_count:     14
    .sgpr_spill_count: 0
    .symbol:         _Z13conv_x_kernelPKfPDF16_.kd
    .uniform_work_group_size: 1
    .uses_dynamic_stack: false
    .vgpr_count:     12
    .vgpr_spill_count: 0
    .wavefront_size: 64
  - .agpr_count:     0
    .args:
      - .actual_access:  read_only
        .address_space:  global
        .offset:         0
        .size:           8
        .value_kind:     global_buffer
      - .actual_access:  read_only
        .address_space:  global
        .offset:         8
        .size:           8
        .value_kind:     global_buffer
      - .actual_access:  read_only
        .address_space:  global
        .offset:         16
        .size:           8
        .value_kind:     global_buffer
      - .actual_access:  read_only
        .address_space:  global
        .offset:         24
        .size:           8
        .value_kind:     global_buffer
      - .actual_access:  write_only
        .address_space:  global
        .offset:         32
        .size:           8
        .value_kind:     global_buffer
      - .actual_access:  write_only
        .address_space:  global
        .offset:         40
        .size:           8
        .value_kind:     global_buffer
      - .actual_access:  read_only
        .address_space:  global
        .offset:         48
        .size:           8
        .value_kind:     global_buffer
      - .actual_access:  write_only
        .address_space:  global
        .offset:         56
        .size:           8
        .value_kind:     global_buffer
    .group_segment_fixed_size: 16640
    .kernarg_segment_align: 8
    .kernarg_segment_size: 64
    .language:       OpenCL C
    .language_version:
      - 2
      - 0
    .max_flat_workgroup_size: 256
    .name:           _Z13conv_w_kernelPKfS0_S0_S0_PDF16_S1_S0_S1_
    .private_segment_fixed_size: 0
    .sgpr_count:     26
    .sgpr_spill_count: 0
    .symbol:         _Z13conv_w_kernelPKfS0_S0_S0_PDF16_S1_S0_S1_.kd
    .uniform_work_group_size: 1
    .uses_dynamic_stack: false
    .vgpr_count:     31
    .vgpr_spill_count: 0
    .wavefront_size: 64
  - .agpr_count:     0
    .args:
      - .actual_access:  read_only
        .address_space:  global
        .offset:         0
        .size:           8
        .value_kind:     global_buffer
      - .actual_access:  read_only
        .address_space:  global
        .offset:         8
        .size:           8
        .value_kind:     global_buffer
      - .actual_access:  write_only
        .address_space:  global
        .offset:         16
        .size:           8
        .value_kind:     global_buffer
    .group_segment_fixed_size: 0
    .kernarg_segment_align: 8
    .kernarg_segment_size: 24
    .language:       OpenCL C
    .language_version:
      - 2
      - 0
    .max_flat_workgroup_size: 512
    .name:           _Z9wo_kernelPKDF16_S0_Pf
    .private_segment_fixed_size: 0
    .sgpr_count:     16
    .sgpr_spill_count: 0
    .symbol:         _Z9wo_kernelPKDF16_S0_Pf.kd
    .uniform_work_group_size: 1
    .uses_dynamic_stack: false
    .vgpr_count:     134
    .vgpr_spill_count: 0
    .wavefront_size: 64
  - .agpr_count:     0
    .args:
      - .address_space:  global
        .offset:         0
        .size:           8
        .value_kind:     global_buffer
      - .address_space:  global
        .offset:         8
        .size:           8
        .value_kind:     global_buffer
      - .actual_access:  write_only
        .address_space:  global
        .offset:         16
        .size:           8
        .value_kind:     global_buffer
      - .actual_access:  write_only
        .address_space:  global
        .offset:         24
        .size:           8
        .value_kind:     global_buffer
    .group_segment_fixed_size: 0
    .kernarg_segment_align: 8
    .kernarg_segment_size: 32
    .language:       OpenCL C
    .language_version:
      - 2
      - 0
    .max_flat_workgroup_size: 512
    .name:           _Z10qkv_kernelPKDF16_S0_PDF16_S1_
    .private_segment_fixed_size: 0
    .sgpr_count:     44
    .sgpr_spill_count: 0
    .symbol:         _Z10qkv_kernelPKDF16_S0_PDF16_S1_.kd
    .uniform_work_group_size: 1
    .uses_dynamic_stack: false
    .vgpr_count:     200
    .vgpr_spill_count: 0
    .wavefront_size: 64
  - .agpr_count:     0
    .args:
      - .actual_access:  read_only
        .address_space:  global
        .offset:         0
        .size:           8
        .value_kind:     global_buffer
      - .actual_access:  read_only
        .address_space:  global
        .offset:         8
        .size:           8
        .value_kind:     global_buffer
      - .actual_access:  read_only
        .address_space:  global
        .offset:         16
        .size:           8
        .value_kind:     global_buffer
      - .actual_access:  read_only
        .address_space:  global
        .offset:         24
        .size:           8
        .value_kind:     global_buffer
      - .actual_access:  read_only
        .address_space:  global
        .offset:         32
        .size:           8
        .value_kind:     global_buffer
      - .actual_access:  read_only
        .address_space:  global
        .offset:         40
        .size:           8
        .value_kind:     global_buffer
      - .actual_access:  read_only
        .address_space:  global
        .offset:         48
        .size:           8
        .value_kind:     global_buffer
      - .actual_access:  write_only
        .address_space:  global
        .offset:         56
        .size:           8
        .value_kind:     global_buffer
      - .actual_access:  write_only
        .address_space:  global
        .offset:         64
        .size:           8
        .value_kind:     global_buffer
      - .actual_access:  write_only
        .address_space:  global
        .offset:         72
        .size:           8
        .value_kind:     global_buffer
    .group_segment_fixed_size: 0
    .kernarg_segment_align: 8
    .kernarg_segment_size: 80
    .language:       OpenCL C
    .language_version:
      - 2
      - 0
    .max_flat_workgroup_size: 512
    .name:           _Z11attn_kernelPKDF16_S0_PKfS2_S2_S2_S2_PfPDF16_S3_
    .private_segment_fixed_size: 0
    .sgpr_count:     44
    .sgpr_spill_count: 0
    .symbol:         _Z11attn_kernelPKDF16_S0_PKfS2_S2_S2_S2_PfPDF16_S3_.kd
    .uniform_work_group_size: 1
    .uses_dynamic_stack: false
    .vgpr_count:     256
    .vgpr_spill_count: 0
    .wavefront_size: 64
